# v9
# speedup vs baseline: 1.0227x; 1.0227x over previous
.LBB0_15:
	s_or_b64 exec, exec, s[22:23]
	s_waitcnt vmcnt(0)
	v_max3_f32 v19, |v14|, 0, |v15|
	v_max3_f32 v19, v19, |v16|, |v17|
	v_max3_f32 v19, v19, |v10|, |v11|
	v_max3_f32 v19, v19, |v12|, |v13|
	ds_bpermute_b32 v23, v1, v19
	s_waitcnt lgkmcnt(0)
	v_max_f32_e32 v23, v23, v23
	v_max_f32_e32 v19, v19, v23
	ds_bpermute_b32 v23, v24, v19
	s_waitcnt lgkmcnt(0)
	v_max_f32_e32 v23, v23, v23
	v_max_f32_e32 v19, v19, v23
	ds_bpermute_b32 v23, v25, v19
	s_waitcnt lgkmcnt(0)
	v_max_f32_e32 v23, v23, v23
	v_max_f32_e32 v19, v19, v23
	ds_bpermute_b32 v23, v26, v19
	s_waitcnt lgkmcnt(0)
	v_max_f32_e32 v23, v23, v23
	v_max_f32_e32 v19, v19, v23
	v_div_scale_f32 v23, s[22:23], v19, v19, s26
	v_rcp_f32_e32 v28, v23
	v_div_scale_f32 v29, vcc, s26, v19, s26
	v_fma_f32 v30, -v23, v28, 1.0
	v_fmac_f32_e32 v28, v30, v28
	v_mul_f32_e32 v30, v29, v28
	v_fma_f32 v31, -v23, v30, v29
	v_fmac_f32_e32 v30, v31, v28
	v_fma_f32 v23, -v23, v30, v29
	v_div_fmas_f32 v23, v23, v28, v30
	v_div_fixup_f32 v23, v23, v19, s26
	v_cmp_lt_f32_e32 vcc, 0, v19
	s_nop 1
	v_cndmask_b32_e32 v23, 0, v23, vcc
	v_mul_f32_e32 v14, v14, v23
	v_mul_f32_e32 v10, v10, v23
	v_mul_f32_e32 v15, v15, v23
	v_mul_f32_e32 v11, v11, v23
	v_rndne_f32_e32 v14, v14
	v_rndne_f32_e32 v10, v10
	v_rndne_f32_e32 v15, v15
	v_rndne_f32_e32 v11, v11
	v_cvt_i32_f32_e32 v14, v14
	v_cvt_i32_f32_e32 v10, v10
	v_cvt_i32_f32_e32 v15, v15
	v_cvt_i32_f32_e32 v11, v11
	v_max_i32_e32 v14, 0xffffff81, v14
	v_max_i32_e32 v10, 0xffffff81, v10
	v_max_i32_e32 v15, 0xffffff81, v15
	v_max_i32_e32 v11, 0xffffff81, v11
	v_add_u32_e32 v14, 0x80, v14
	v_add_u32_e32 v10, 0x80, v10
	v_add_u32_e32 v15, 0x80, v15
	v_add_u32_e32 v11, 0x80, v11
	v_min_u32_e32 v14, 0xff, v14
	v_min_u32_e32 v10, 0xff, v10
	v_min_u32_e32 v15, 0xff, v15
	v_min_u32_e32 v11, 0xff, v11
	v_lshl_or_b32 v14, v15, 8, v14
	v_lshl_or_b32 v11, v11, 8, v10
	v_mul_f32_e32 v10, v16, v23
	v_mul_f32_e32 v12, v12, v23
	v_mul_f32_e32 v15, v17, v23
	v_mul_f32_e32 v13, v13, v23
	v_rndne_f32_e32 v10, v10
	v_rndne_f32_e32 v12, v12
	v_rndne_f32_e32 v15, v15
	v_rndne_f32_e32 v13, v13
	v_cvt_i32_f32_e32 v10, v10
	v_cvt_i32_f32_e32 v12, v12
	v_cvt_i32_f32_e32 v15, v15
	v_cvt_i32_f32_e32 v13, v13
	v_max_i32_e32 v10, 0xffffff81, v10
	v_max_i32_e32 v12, 0xffffff81, v12
	v_max_i32_e32 v15, 0xffffff81, v15
	v_max_i32_e32 v13, 0xffffff81, v13
	v_add_u32_e32 v10, 0x80, v10
	v_add_u32_e32 v12, 0x80, v12
	v_add_u32_e32 v15, 0x80, v15
	v_add_u32_e32 v13, 0x80, v13
	v_min_u32_sdwa v10, v10, s27 dst_sel:WORD_1 dst_unused:UNUSED_PAD src0_sel:DWORD src1_sel:DWORD
	v_min_u32_sdwa v12, v12, s27 dst_sel:WORD_1 dst_unused:UNUSED_PAD src0_sel:DWORD src1_sel:DWORD
	v_min_u32_sdwa v15, v15, s27 dst_sel:BYTE_3 dst_unused:UNUSED_PAD src0_sel:DWORD src1_sel:DWORD
	v_min_u32_sdwa v13, v13, s27 dst_sel:BYTE_3 dst_unused:UNUSED_PAD src0_sel:DWORD src1_sel:DWORD
	v_or3_b32 v10, v14, v10, v15
	v_or3_b32 v11, v11, v12, v13
	global_store_dwordx2 v[20:21], v[10:11], off offset:-4
	s_and_saveexec_b64 s[22:23], s[6:7]
	s_cbranch_execz .LBB0_17
	v_ashrrev_i32_e32 v10, 4, v18
	v_ashrrev_i32_e32 v11, 31, v10
	v_mul_f32_e32 v12, 0x41010204, v19
	v_lshl_add_u64 v[10:11], v[10:11], 2, s[12:13]
	global_store_dword v[10:11], v12, off
.LBB0_17:
	s_or_b64 exec, exec, s[22:23]
	s_and_saveexec_b64 s[22:23], s[4:5]
	s_cbranch_execz .LBB0_12
	v_max3_f32 v10, |v2|, 0, |v3|
	v_max3_f32 v10, v10, |v4|, |v5|
	v_max3_f32 v10, v10, |v6|, |v7|
	v_max3_f32 v10, v10, |v8|, |v9|
	ds_bpermute_b32 v11, v1, v10
	v_ashrrev_i32_e32 v23, 31, v22
	s_waitcnt lgkmcnt(0)
	v_max_f32_e32 v11, v11, v11
	v_max_f32_e32 v10, v10, v11
	ds_bpermute_b32 v11, v24, v10
	s_waitcnt lgkmcnt(0)
	v_max_f32_e32 v11, v11, v11
	v_max_f32_e32 v10, v10, v11
	ds_bpermute_b32 v11, v25, v10
	s_waitcnt lgkmcnt(0)
	v_max_f32_e32 v11, v11, v11
	v_max_f32_e32 v10, v10, v11
	ds_bpermute_b32 v11, v26, v10
	s_waitcnt lgkmcnt(0)
	v_max_f32_e32 v11, v11, v11
	v_max_f32_e32 v10, v10, v11
	v_div_scale_f32 v11, s[4:5], v10, v10, s26
	v_rcp_f32_e32 v12, v11
	v_div_scale_f32 v13, vcc, s26, v10, s26
	v_fma_f32 v14, -v11, v12, 1.0
	v_fmac_f32_e32 v12, v14, v12
	v_mul_f32_e32 v14, v13, v12
	v_fma_f32 v15, -v11, v14, v13
	v_fmac_f32_e32 v14, v15, v12
	v_fma_f32 v11, -v11, v14, v13
	v_div_fmas_f32 v11, v11, v12, v14
	v_div_fixup_f32 v11, v11, v10, s26
	v_cmp_lt_f32_e32 vcc, 0, v10
	s_nop 1
	v_cndmask_b32_e32 v11, 0, v11, vcc
	v_mul_f32_e32 v2, v2, v11
	v_mul_f32_e32 v6, v6, v11
	v_mul_f32_e32 v3, v3, v11
	v_mul_f32_e32 v7, v7, v11
	v_rndne_f32_e32 v2, v2
	v_rndne_f32_e32 v6, v6
	v_rndne_f32_e32 v3, v3
	v_rndne_f32_e32 v7, v7
	v_cvt_i32_f32_e32 v2, v2
	v_cvt_i32_f32_e32 v6, v6
	v_cvt_i32_f32_e32 v3, v3
	v_cvt_i32_f32_e32 v7, v7
	v_max_i32_e32 v2, 0xffffff81, v2
	v_max_i32_e32 v6, 0xffffff81, v6
	v_max_i32_e32 v3, 0xffffff81, v3
	v_max_i32_e32 v7, 0xffffff81, v7
	v_add_u32_e32 v2, 0x80, v2
	v_add_u32_e32 v6, 0x80, v6
	v_add_u32_e32 v3, 0x80, v3
	v_add_u32_e32 v7, 0x80, v7
	v_min_u32_e32 v2, 0xff, v2
	v_min_u32_e32 v6, 0xff, v6
	v_min_u32_e32 v3, 0xff, v3
	v_min_u32_e32 v7, 0xff, v7
	v_lshl_or_b32 v2, v3, 8, v2
	v_lshl_or_b32 v3, v7, 8, v6
	v_mul_f32_e32 v4, v4, v11
	v_mul_f32_e32 v6, v8, v11
	v_mul_f32_e32 v5, v5, v11
	v_mul_f32_e32 v7, v9, v11
	v_rndne_f32_e32 v4, v4
	v_rndne_f32_e32 v6, v6
	v_rndne_f32_e32 v5, v5
	v_rndne_f32_e32 v7, v7
	v_cvt_i32_f32_e32 v4, v4
	v_cvt_i32_f32_e32 v6, v6
	v_cvt_i32_f32_e32 v5, v5
	v_cvt_i32_f32_e32 v7, v7
	v_max_i32_e32 v4, 0xffffff81, v4
	v_max_i32_e32 v6, 0xffffff81, v6
	v_max_i32_e32 v5, 0xffffff81, v5
	v_max_i32_e32 v7, 0xffffff81, v7
	v_add_u32_e32 v4, 0x80, v4
	v_add_u32_e32 v6, 0x80, v6
	v_add_u32_e32 v5, 0x80, v5
	v_add_u32_e32 v7, 0x80, v7
	v_min_u32_sdwa v4, v4, s27 dst_sel:WORD_1 dst_unused:UNUSED_PAD src0_sel:DWORD src1_sel:DWORD
	v_min_u32_sdwa v6, v6, s27 dst_sel:WORD_1 dst_unused:UNUSED_PAD src0_sel:DWORD src1_sel:DWORD
	v_min_u32_sdwa v5, v5, s27 dst_sel:BYTE_3 dst_unused:UNUSED_PAD src0_sel:DWORD src1_sel:DWORD
	v_min_u32_sdwa v7, v7, s27 dst_sel:BYTE_3 dst_unused:UNUSED_PAD src0_sel:DWORD src1_sel:DWORD
	v_or3_b32 v2, v2, v4, v5
	v_or3_b32 v3, v3, v6, v7
	v_lshl_add_u64 v[4:5], v[22:23], 3, s[8:9]
	global_store_dwordx2 v[4:5], v[2:3], off
	s_and_b64 exec, exec, s[6:7]
	s_cbranch_execz .LBB0_12
	v_ashrrev_i32_e32 v2, 4, v22
	v_ashrrev_i32_e32 v3, 31, v2
	v_mul_f32_e32 v4, 0x41010204, v10
	v_lshl_add_u64 v[2:3], v[2:3], 2, s[12:13]
	global_store_dword v[2:3], v4, off
	s_branch .LBB0_12

.LBB2_9:
	v_max_i32_e32 v19, 1, v28
	v_cvt_f32_u32_e32 v19, v19
	v_add_u32_e32 v21, s20, v76
	v_div_scale_f32 v20, s[14:15], v19, v19, 1.0
	v_rcp_f32_e32 v27, v20
	v_div_scale_f32 v28, vcc, 1.0, v19, 1.0
	v_pk_add_f32 v[2:3], v[2:3], v[18:19] op_sel_hi:[1,0] neg_lo:[0,1] neg_hi:[0,1]
	v_fma_f32 v29, -v20, v27, 1.0
	v_fmac_f32_e32 v27, v29, v27
	v_mul_f32_e32 v29, v28, v27
	v_fma_f32 v30, -v20, v29, v28
	v_fmac_f32_e32 v29, v30, v27
	v_fma_f32 v20, -v20, v29, v28
	v_div_fmas_f32 v20, v20, v27, v29
	v_div_fixup_f32 v20, v20, v19, 1.0
	v_mul_f32_e32 v20, 0x3a800000, v20
	v_pk_mul_f32 v[2:3], v[20:21], v[2:3] op_sel_hi:[0,1]
	v_pk_add_f32 v[14:15], v[14:15], v[18:19] op_sel_hi:[1,0] neg_lo:[0,1] neg_hi:[0,1]
	v_cvt_pk_f16_f32 v31, v2, v3
	v_xor_b32_e32 v2, v21, v0
	v_pk_add_f32 v[16:17], v[16:17], v[18:19] op_sel_hi:[1,0] neg_lo:[0,1] neg_hi:[0,1]
	v_pk_mul_f32 v[14:15], v[20:21], v[14:15] op_sel_hi:[0,1]
	v_pk_add_f32 v[4:5], v[4:5], v[18:19] op_sel_hi:[1,0] neg_lo:[0,1] neg_hi:[0,1]
	v_lshlrev_b32_e32 v2, 4, v2
	v_pk_mul_f32 v[16:17], v[20:21], v[16:17] op_sel_hi:[0,1]
	v_cvt_pk_f16_f32 v29, v14, v15
	v_pk_mul_f32 v[4:5], v[20:21], v[4:5] op_sel_hi:[0,1]
	v_and_b32_e32 v2, 0xf0, v2
	v_add_u32_e32 v14, s18, v21
	v_cvt_pk_f16_f32 v28, v16, v17
	v_cvt_pk_f16_f32 v30, v4, v5
	v_lshl_or_b32 v16, v21, 8, v2
	v_cmp_gt_i32_e32 vcc, s16, v14
	v_mov_b32_e32 v2, 0
	v_mov_b32_e32 v3, 0
	v_mov_b32_e32 v4, 0
	v_mov_b32_e32 v5, 0
	ds_write_b128 v16, v[28:31]
	s_and_saveexec_b64 s[14:15], vcc
	s_cbranch_execz .LBB2_2
	v_ashrrev_i32_e32 v15, 31, v14
	v_lshlrev_b64 v[2:3], 9, v[14:15]
	v_lshl_add_u64 v[14:15], v[12:13], 0, v[2:3]
	global_load_dwordx4 v[2:5], v[14:15], off
	global_load_dwordx4 v[18:21], v[14:15], off offset:16
	s_waitcnt vmcnt(1)
	v_cvt_f16_f32_e32 v2, v2
	s_waitcnt vmcnt(0)
	v_cvt_f16_f32_e32 v15, v21
	v_cvt_pk_f16_f32 v14, v3, v4
	v_cvt_pk_f16_f32 v4, v5, v18
	v_cvt_pk_f16_f32 v5, v19, v20
	v_alignbit_b32 v3, v4, v14, 16
	v_alignbit_b32 v4, v5, v4, 16
	v_pack_b32_f16 v2, v2, v14
	v_alignbit_b32 v5, v15, v5, 16
	s_branch .LBB2_2

.LBB2_35:
	s_waitcnt vmcnt(10)
	v_cvt_pk_f16_f32 v10, v61, v62
	v_perm_b32 v11, v40, v38, s23
	v_dot2c_f32_f16_e32 v60, v11, v10
	v_perm_b32 v11, v40, v38, s24
	v_dot2c_f32_f16_e32 v42, v11, v10
	v_perm_b32 v11, v40, v38, s25
	v_dot2c_f32_f16_e32 v43, v11, v10
	v_perm_b32 v11, v40, v38, s26
	v_dot2c_f32_f16_e32 v36, v11, v10
	v_perm_b32 v11, v41, v39, s23
	v_dot2c_f32_f16_e32 v37, v11, v10
	v_perm_b32 v11, v41, v39, s24
	v_dot2c_f32_f16_e32 v30, v11, v10
	v_perm_b32 v11, v41, v39, s25
	v_dot2c_f32_f16_e32 v31, v11, v10
	v_perm_b32 v11, v41, v39, s26
	v_dot2c_f32_f16_e32 v53, v11, v10
	v_dot2c_f32_f16_e32 v45, 0x3c003c00, v10
	s_waitcnt vmcnt(8)
	v_cvt_pk_f16_f32 v10, v58, v59
	v_perm_b32 v11, v34, v32, s23
	v_dot2c_f32_f16_e32 v60, v11, v10
	v_perm_b32 v11, v34, v32, s24
	v_dot2c_f32_f16_e32 v42, v11, v10
	v_perm_b32 v11, v34, v32, s25
	v_dot2c_f32_f16_e32 v43, v11, v10
	v_perm_b32 v11, v34, v32, s26
	v_dot2c_f32_f16_e32 v36, v11, v10
	v_perm_b32 v11, v35, v33, s23
	v_dot2c_f32_f16_e32 v37, v11, v10
	v_perm_b32 v11, v35, v33, s24
	v_dot2c_f32_f16_e32 v30, v11, v10
	v_perm_b32 v11, v35, v33, s25
	v_dot2c_f32_f16_e32 v31, v11, v10
	v_perm_b32 v11, v35, v33, s26
	s_add_i32 s5, s5, 1
	v_dot2c_f32_f16_e32 v53, v11, v10
	s_cmp_lg_u32 s5, s4
	v_dot2c_f32_f16_e32 v45, 0x3c003c00, v10
	s_cbranch_scc1 .LBB2_43
	v_cmp_gt_i32_e32 vcc, 15, v18
	s_and_saveexec_b64 s[4:5], vcc
	s_cbranch_execz .LBB2_38
	v_max_i32_e32 v10, 1, v44
	v_cvt_f32_u32_e32 v10, v10
	v_rcp_iflag_f32_e32 v44, v10
	s_nop 0
	v_pk_mul_f32 v[10:11], v[44:45], s[2:3]
	s_nop 0
	v_mul_f32_e32 v14, 0x4b800000, v10
	v_pk_mul_f32 v[16:17], v[10:11], v[10:11] op_sel:[0,1] op_sel_hi:[1,0]
	s_nop 0
	v_fma_mixlo_f16 v15, v60, v14, v16
	v_pk_fma_f32 v[10:11], v[42:43], v[14:15], v[16:17] op_sel_hi:[1,0,0]
	v_pk_fma_f32 v[12:13], v[36:37], v[14:15], v[16:17] op_sel_hi:[1,0,0]
	v_pk_fma_f32 v[30:31], v[30:31], v[14:15], v[16:17] op_sel_hi:[1,0,0]
	v_cvt_pk_f16_f32 v11, v10, v11
	v_cvt_pk_f16_f32 v12, v12, v13
	v_cvt_pk_f16_f32 v13, v30, v31
	v_pack_b32_f16 v10, v15, v11
	v_alignbit_b32 v11, v12, v11, 16
	v_alignbit_b32 v12, v13, v12, 16
	v_lshrrev_b32_e32 v13, 16, v13
	v_fma_mixhi_f16 v13, v53, v14, v16
	v_add_u32_e32 v14, v18, v77
	v_xor_b32_e32 v15, v14, v0
	v_lshlrev_b32_e32 v15, 4, v15
	v_and_b32_e32 v15, 0xf0, v15
	v_lshl_or_b32 v14, v14, 8, v15
	ds_write_b128 v14, v[10:13]

.LBB2_43:
	s_lshl_b32 s28, s27, 2
	v_add_u32_e32 v10, s28, v3
	v_lshl_add_u32 v10, v10, 2, v2
	ds_read_b32 v11, v10 offset:15360
	ds_read_b32 v12, v10 offset:15364
	ds_read_b32 v13, v10 offset:15368
	ds_read_b32 v10, v10 offset:15372
	v_cmp_lt_i32_e32 vcc, s28, v5
	s_or_b32 s29, s28, 1
	s_add_i32 s27, s27, 1
	s_waitcnt lgkmcnt(3)
	v_cndmask_b32_e32 v11, v9, v11, vcc
	v_cmp_lt_i32_e32 vcc, s29, v5
	s_or_b32 s29, s28, 2
	s_or_b32 s28, s28, 3
	s_waitcnt lgkmcnt(2)
	v_cndmask_b32_e32 v12, v9, v12, vcc
	v_cmp_lt_i32_e32 vcc, s29, v5
	v_lshl_or_b32 v14, v11, 7, v66
	v_lshlrev_b32_e32 v11, 2, v11
	s_waitcnt lgkmcnt(1)
	v_cndmask_b32_e32 v13, v9, v13, vcc
	v_cmp_lt_i32_e32 vcc, s28, v5
	v_lshl_or_b32 v15, v12, 7, v66
	v_lshl_or_b32 v16, v13, 7, v66
	s_waitcnt lgkmcnt(0)
	v_cndmask_b32_e32 v10, v9, v10, vcc
	v_lshl_or_b32 v17, v10, 7, v66
	global_load_dwordx2 v[38:39], v14, s[10:11]
	global_load_dwordx2 v[40:41], v15, s[10:11]
	global_load_dwordx2 v[32:33], v16, s[10:11]
	global_load_dwordx2 v[34:35], v17, s[10:11]
	v_lshlrev_b32_e32 v12, 2, v12
	v_lshlrev_b32_e32 v13, 2, v13
	v_lshlrev_b32_e32 v10, 2, v10
	global_load_dword v61, v11, s[12:13]
	global_load_dword v62, v12, s[12:13]
	global_load_dword v58, v13, s[12:13]
	global_load_dword v59, v10, s[12:13]
	s_cmp_lg_u32 s27, s21
	s_cbranch_scc1 .LBB2_49
	s_cmp_eq_u32 s20, 0
	s_cbranch_scc1 .LBB2_47
	s_add_i32 s27, s20, 1
	s_mov_b32 s20, 2
	s_cmp_eq_u32 s27, 2
	v_mov_b32_e32 v3, v7
	v_mov_b32_e32 v5, v51
	s_mov_b32 s21, s16
	s_cbranch_scc1 .LBB2_48
	s_cmp_eq_u32 s27, 3
	s_cselect_b64 vcc, -1, 0
	s_and_b64 s[20:21], vcc, exec
	v_cndmask_b32_e32 v5, 0, v52, vcc
	s_cselect_b32 s21, s6, 0x7fffffff
	s_mov_b32 s20, s27
	v_mov_b32_e32 v3, v8
	s_branch .LBB2_48

.LBB2_49:
	s_waitcnt vmcnt(10)
	v_cvt_pk_f16_f32 v10, v56, v57
	v_perm_b32 v11, v28, v26, s23
	v_dot2c_f32_f16_e32 v60, v11, v10
	v_perm_b32 v11, v28, v26, s24
	v_dot2c_f32_f16_e32 v42, v11, v10
	v_perm_b32 v11, v28, v26, s25
	v_dot2c_f32_f16_e32 v43, v11, v10
	v_perm_b32 v11, v28, v26, s26
	v_dot2c_f32_f16_e32 v36, v11, v10
	v_perm_b32 v11, v29, v27, s23
	v_dot2c_f32_f16_e32 v37, v11, v10
	v_perm_b32 v11, v29, v27, s24
	v_dot2c_f32_f16_e32 v30, v11, v10
	v_perm_b32 v11, v29, v27, s25
	v_dot2c_f32_f16_e32 v31, v11, v10
	v_perm_b32 v11, v29, v27, s26
	v_dot2c_f32_f16_e32 v53, v11, v10
	v_dot2c_f32_f16_e32 v45, 0x3c003c00, v10
	s_waitcnt vmcnt(8)
	v_cvt_pk_f16_f32 v10, v54, v55
	v_perm_b32 v11, v24, v22, s23
	v_dot2c_f32_f16_e32 v60, v11, v10
	v_perm_b32 v11, v24, v22, s24
	v_dot2c_f32_f16_e32 v42, v11, v10
	v_perm_b32 v11, v24, v22, s25
	v_dot2c_f32_f16_e32 v43, v11, v10
	v_perm_b32 v11, v24, v22, s26
	v_dot2c_f32_f16_e32 v36, v11, v10
	v_perm_b32 v11, v25, v23, s23
	v_dot2c_f32_f16_e32 v37, v11, v10
	v_perm_b32 v11, v25, v23, s24
	v_dot2c_f32_f16_e32 v30, v11, v10
	v_perm_b32 v11, v25, v23, s25
	v_dot2c_f32_f16_e32 v31, v11, v10
	v_perm_b32 v11, v25, v23, s26
	s_add_i32 s5, s5, 1
	v_dot2c_f32_f16_e32 v53, v11, v10
	s_cmp_lg_u32 s5, s4
	v_dot2c_f32_f16_e32 v45, 0x3c003c00, v10
	s_cbranch_scc1 .LBB2_57
	v_cmp_gt_i32_e32 vcc, 15, v18
	s_and_saveexec_b64 s[4:5], vcc
	s_cbranch_execz .LBB2_52
	v_max_i32_e32 v10, 1, v44
	v_cvt_f32_u32_e32 v10, v10
	v_rcp_iflag_f32_e32 v44, v10
	s_nop 0
	v_pk_mul_f32 v[10:11], v[44:45], s[2:3]
	s_nop 0
	v_mul_f32_e32 v14, 0x4b800000, v10
	v_pk_mul_f32 v[16:17], v[10:11], v[10:11] op_sel:[0,1] op_sel_hi:[1,0]
	s_nop 0
	v_fma_mixlo_f16 v15, v60, v14, v16
	v_pk_fma_f32 v[10:11], v[42:43], v[14:15], v[16:17] op_sel_hi:[1,0,0]
	v_pk_fma_f32 v[12:13], v[36:37], v[14:15], v[16:17] op_sel_hi:[1,0,0]
	v_pk_fma_f32 v[22:23], v[30:31], v[14:15], v[16:17] op_sel_hi:[1,0,0]
	v_cvt_pk_f16_f32 v11, v10, v11
	v_cvt_pk_f16_f32 v12, v12, v13
	v_cvt_pk_f16_f32 v13, v22, v23
	v_pack_b32_f16 v10, v15, v11
	v_alignbit_b32 v11, v12, v11, 16
	v_alignbit_b32 v12, v13, v12, 16
	v_lshrrev_b32_e32 v13, 16, v13
	v_fma_mixhi_f16 v13, v53, v14, v16
	v_add_u32_e32 v14, v18, v77
	v_xor_b32_e32 v15, v14, v0
	v_lshlrev_b32_e32 v15, 4, v15
	v_and_b32_e32 v15, 0xf0, v15
	v_lshl_or_b32 v14, v14, 8, v15
	ds_write_b128 v14, v[10:13]

.LBB2_57:
	s_lshl_b32 s28, s27, 2
	v_add_u32_e32 v10, s28, v3
	v_lshl_add_u32 v10, v10, 2, v2
	ds_read_b32 v11, v10 offset:15360
	ds_read_b32 v12, v10 offset:15364
	ds_read_b32 v13, v10 offset:15368
	ds_read_b32 v10, v10 offset:15372
	v_cmp_lt_i32_e32 vcc, s28, v5
	s_or_b32 s29, s28, 1
	s_add_i32 s27, s27, 1
	s_waitcnt lgkmcnt(3)
	v_cndmask_b32_e32 v11, v9, v11, vcc
	v_cmp_lt_i32_e32 vcc, s29, v5
	s_or_b32 s29, s28, 2
	s_or_b32 s28, s28, 3
	s_waitcnt lgkmcnt(2)
	v_cndmask_b32_e32 v12, v9, v12, vcc
	v_cmp_lt_i32_e32 vcc, s29, v5
	v_lshl_or_b32 v14, v11, 7, v66
	v_lshlrev_b32_e32 v11, 2, v11
	s_waitcnt lgkmcnt(1)
	v_cndmask_b32_e32 v13, v9, v13, vcc
	v_cmp_lt_i32_e32 vcc, s28, v5
	v_lshl_or_b32 v15, v12, 7, v66
	v_lshl_or_b32 v16, v13, 7, v66
	s_waitcnt lgkmcnt(0)
	v_cndmask_b32_e32 v10, v9, v10, vcc
	v_lshl_or_b32 v17, v10, 7, v66
	global_load_dwordx2 v[26:27], v14, s[10:11]
	global_load_dwordx2 v[28:29], v15, s[10:11]
	global_load_dwordx2 v[22:23], v16, s[10:11]
	global_load_dwordx2 v[24:25], v17, s[10:11]
	v_lshlrev_b32_e32 v12, 2, v12
	v_lshlrev_b32_e32 v13, 2, v13
	v_lshlrev_b32_e32 v10, 2, v10
	global_load_dword v56, v11, s[12:13]
	global_load_dword v57, v12, s[12:13]
	global_load_dword v54, v13, s[12:13]
	global_load_dword v55, v10, s[12:13]
	s_cmp_lg_u32 s27, s21
	s_cbranch_scc1 .LBB2_34
	s_cmp_eq_u32 s20, 0
	s_cbranch_scc1 .LBB2_32
	s_add_i32 s27, s20, 1
	s_mov_b32 s20, 2
	s_cmp_eq_u32 s27, 2
	v_mov_b32_e32 v3, v7
	v_mov_b32_e32 v5, v51
	s_mov_b32 s21, s16
	s_cbranch_scc1 .LBB2_33
	s_cmp_eq_u32 s27, 3
	s_cselect_b64 vcc, -1, 0
	s_and_b64 s[20:21], vcc, exec
	v_cndmask_b32_e32 v5, 0, v52, vcc
	s_cselect_b32 s21, s6, 0x7fffffff
	s_mov_b32 s20, s27
	v_mov_b32_e32 v3, v8
	s_branch .LBB2_33

.LBB2_71:
	s_or_b64 exec, exec, s[0:1]
	v_lshlrev_b32_e32 v14, 2, v72
	v_lshlrev_b32_e32 v10, 4, v73
	v_or_b32_e32 v12, v14, v1
	s_movk_i32 s8, 0x110
	v_mad_u32_u24 v2, v12, s8, v10
	s_waitcnt lgkmcnt(0)
	s_barrier
	ds_read_b128 v[2:5], v2
	v_mov_b32_e32 v67, 0
	v_mov_b32_e32 v11, v67
	v_lshl_add_u64 v[8:9], s[4:5], 0, v[10:11]
	v_add_u32_e32 v12, s18, v12
	s_waitcnt lgkmcnt(0)
	v_cvt_f32_f16_e32 v13, v2
	v_cvt_f32_f16_sdwa v15, v2 dst_sel:DWORD dst_unused:UNUSED_PAD src0_sel:WORD_1
	v_cvt_f32_f16_e32 v16, v3
	v_cvt_f32_f16_sdwa v17, v3 dst_sel:DWORD dst_unused:UNUSED_PAD src0_sel:WORD_1
	v_cvt_f32_f16_e32 v19, v4
	v_cvt_f32_f16_sdwa v20, v4 dst_sel:DWORD dst_unused:UNUSED_PAD src0_sel:WORD_1
	v_cvt_f32_f16_e32 v21, v5
	v_cvt_f32_f16_sdwa v22, v5 dst_sel:DWORD dst_unused:UNUSED_PAD src0_sel:WORD_1
	v_max3_f32 v11, v13, 0, v15
	v_max3_f32 v11, v11, v16, v17
	v_max3_f32 v11, v11, v19, v20
	v_max3_f32 v11, v11, v21, v22
	v_cmp_ne_u32_e64 s[0:1], 15, v72
	s_mov_b32 s4, 0x186a0
	v_mov_b32_dpp v18, v11 quad_perm:[1,0,3,2] row_mask:0xf bank_mask:0xf bound_ctrl:1
	v_max_f32_e32 v18, v18, v18
	v_max_f32_e32 v11, v11, v18
	v_lshl_add_u64 v[6:7], s[6:7], 0, v[66:67]
	v_cmp_eq_u32_e32 vcc, 0, v73
	v_mov_b32_dpp v18, v11 quad_perm:[2,3,0,1] row_mask:0xf bank_mask:0xf bound_ctrl:1
	v_max_f32_e32 v18, v18, v18
	v_max_f32_e32 v11, v11, v18
	s_nop 1
	v_mov_b32_dpp v18, v11 row_half_mirror row_mask:0xf bank_mask:0xf bound_ctrl:1
	v_max_f32_e32 v18, v18, v18
	v_max_f32_e32 v18, v11, v18
	v_mov_b32_e32 v11, 0x186a0
	v_cndmask_b32_e64 v12, v11, v12, s[0:1]
	v_mov_b32_dpp v23, v18 row_mirror row_mask:0xf bank_mask:0xf bound_ctrl:1
	v_cmp_gt_i32_e64 s[0:1], s4, v12
	s_and_saveexec_b64 s[2:3], s[0:1]
	s_cbranch_execz .LBB2_74
	v_max_f32_e32 v23, v23, v23
	v_max_f32_e32 v18, v18, v18
	v_max_f32_e32 v18, v18, v23
	v_rcp_f32_e32 v23, v18
	v_cmp_lt_f32_e64 s[0:1], 0, v18
	v_mul_f32_e32 v23, 0x437f0000, v23
	s_nop 0
	v_cndmask_b32_e64 v23, 0, v23, s[0:1]
	v_mul_f32_e32 v13, v23, v13
	v_mul_f32_e32 v19, v23, v19
	v_mul_f32_e32 v15, v23, v15
	v_rndne_f32_e32 v13, v13
	v_mul_f32_e32 v20, v23, v20
	v_rndne_f32_e32 v19, v19
	v_mul_f32_e32 v16, v23, v16
	v_rndne_f32_e32 v15, v15
	v_cvt_pk_u8_f32 v13, v13, 0, 0
	v_mul_f32_e32 v21, v23, v21
	v_rndne_f32_e32 v20, v20
	v_cvt_pk_u8_f32 v19, v19, 0, 0
	v_mul_f32_e32 v17, v23, v17
	v_rndne_f32_e32 v16, v16
	v_cvt_pk_u8_f32 v13, v15, 1, v13
	v_mul_f32_e32 v22, v23, v22
	v_rndne_f32_e32 v21, v21
	v_cvt_pk_u8_f32 v19, v20, 1, v19
	v_rndne_f32_e32 v17, v17
	v_cvt_pk_u8_f32 v13, v16, 2, v13
	v_rndne_f32_e32 v22, v22
	v_cvt_pk_u8_f32 v19, v21, 2, v19
	v_cvt_pk_u8_f32 v20, v17, 3, v13
	v_ashrrev_i32_e32 v13, 31, v12
	v_cvt_pk_u8_f32 v21, v22, 3, v19
	v_lshlrev_b64 v[22:23], 8, v[12:13]
	v_lshlrev_b64 v[16:17], 7, v[12:13]
	v_lshl_add_u64 v[22:23], v[8:9], 0, v[22:23]
	global_store_dwordx4 v[22:23], v[2:5], off
	s_nop 1
	v_lshl_add_u64 v[2:3], v[6:7], 0, v[16:17]
	global_store_dwordx2 v[2:3], v[20:21], off
	s_and_b64 exec, exec, vcc
	s_cbranch_execz .LBB2_74
	v_lshl_add_u64 v[2:3], v[12:13], 2, s[14:15]
	v_mul_f32_e32 v4, 0x40808081, v18
	global_store_dword v[2:3], v4, off
.LBB2_74:
	s_or_b64 exec, exec, s[2:3]
	v_add3_u32 v12, v14, v1, 16
	v_mad_u32_u24 v2, v12, s8, v10
	ds_read_b128 v[2:5], v2
	s_movk_i32 s0, 0x2c0
	v_add_u32_e32 v12, s18, v12
	v_cmp_gt_u32_e64 s[0:1], s0, v0
	s_waitcnt lgkmcnt(0)
	v_cvt_f32_f16_e32 v13, v2
	v_cvt_f32_f16_sdwa v15, v2 dst_sel:DWORD dst_unused:UNUSED_PAD src0_sel:WORD_1
	v_cvt_f32_f16_e32 v16, v3
	v_cvt_f32_f16_sdwa v17, v3 dst_sel:DWORD dst_unused:UNUSED_PAD src0_sel:WORD_1
	v_cvt_f32_f16_e32 v18, v4
	v_cvt_f32_f16_sdwa v19, v4 dst_sel:DWORD dst_unused:UNUSED_PAD src0_sel:WORD_1
	v_cvt_f32_f16_e32 v20, v5
	v_cvt_f32_f16_sdwa v21, v5 dst_sel:DWORD dst_unused:UNUSED_PAD src0_sel:WORD_1
	v_max3_f32 v22, v13, 0, v15
	v_max3_f32 v22, v22, v16, v17
	v_max3_f32 v22, v22, v18, v19
	v_max3_f32 v22, v22, v20, v21
	v_cndmask_b32_e64 v12, v11, v12, s[0:1]
	v_cmp_gt_i32_e64 s[0:1], s4, v12
	v_mov_b32_dpp v23, v22 quad_perm:[1,0,3,2] row_mask:0xf bank_mask:0xf bound_ctrl:1
	v_max_f32_e32 v23, v23, v23
	v_max_f32_e32 v22, v22, v23
	s_nop 1
	v_mov_b32_dpp v23, v22 quad_perm:[2,3,0,1] row_mask:0xf bank_mask:0xf bound_ctrl:1
	v_max_f32_e32 v23, v23, v23
	v_max_f32_e32 v22, v22, v23
	s_nop 1
	v_mov_b32_dpp v23, v22 row_half_mirror row_mask:0xf bank_mask:0xf bound_ctrl:1
	v_max_f32_e32 v23, v23, v23
	v_max_f32_e32 v22, v22, v23
	s_nop 1
	v_mov_b32_dpp v23, v22 row_mirror row_mask:0xf bank_mask:0xf bound_ctrl:1
	s_and_saveexec_b64 s[2:3], s[0:1]
	s_cbranch_execz .LBB2_77
	v_max_f32_e32 v11, v23, v23
	v_max_f32_e32 v22, v22, v22
	v_max_f32_e32 v11, v22, v11
	v_rcp_f32_e32 v22, v11
	v_cmp_lt_f32_e64 s[0:1], 0, v11
	v_mul_f32_e32 v22, 0x437f0000, v22
	s_nop 0
	v_cndmask_b32_e64 v22, 0, v22, s[0:1]
	v_mul_f32_e32 v18, v22, v18
	v_mul_f32_e32 v13, v22, v13
	v_mul_f32_e32 v19, v22, v19
	v_rndne_f32_e32 v18, v18
	v_mul_f32_e32 v15, v22, v15
	v_rndne_f32_e32 v13, v13
	v_mul_f32_e32 v20, v22, v20
	v_rndne_f32_e32 v19, v19
	v_cvt_pk_u8_f32 v18, v18, 0, 0
	v_mul_f32_e32 v16, v22, v16
	v_rndne_f32_e32 v15, v15
	v_cvt_pk_u8_f32 v13, v13, 0, 0
	v_mul_f32_e32 v21, v22, v21
	v_rndne_f32_e32 v20, v20
	v_cvt_pk_u8_f32 v18, v19, 1, v18
	v_mul_f32_e32 v17, v22, v17
	v_rndne_f32_e32 v16, v16
	v_cvt_pk_u8_f32 v13, v15, 1, v13
	v_rndne_f32_e32 v21, v21
	v_cvt_pk_u8_f32 v18, v20, 2, v18
	v_rndne_f32_e32 v17, v17
	v_cvt_pk_u8_f32 v13, v16, 2, v13
	v_cvt_pk_u8_f32 v19, v21, 3, v18
	v_cvt_pk_u8_f32 v18, v17, 3, v13
	v_ashrrev_i32_e32 v13, 31, v12
	v_lshlrev_b64 v[20:21], 8, v[12:13]
	v_lshlrev_b64 v[16:17], 7, v[12:13]
	v_lshl_add_u64 v[20:21], v[8:9], 0, v[20:21]
	global_store_dwordx4 v[20:21], v[2:5], off
	s_nop 1
	v_lshl_add_u64 v[2:3], v[6:7], 0, v[16:17]
	global_store_dwordx2 v[2:3], v[18:19], off
	s_and_b64 exec, exec, vcc
	s_cbranch_execz .LBB2_77
	v_lshl_add_u64 v[2:3], v[12:13], 2, s[14:15]
	v_mul_f32_e32 v4, 0x40808081, v11
	global_store_dword v[2:3], v4, off
.LBB2_77:
	s_or_b64 exec, exec, s[2:3]
	v_add_u32_e32 v2, v14, v1
	v_or_b32_e32 v11, 32, v2
	s_movk_i32 s5, 0x110
	v_mad_u32_u24 v2, v11, s5, v10
	ds_read_b128 v[2:5], v2
	v_add_u32_e32 v12, s18, v11
	s_movk_i32 s0, 0x1c0
	v_cmp_gt_u32_e64 s[0:1], s0, v0
	s_waitcnt lgkmcnt(0)
	v_cvt_f32_f16_e32 v13, v2
	v_cvt_f32_f16_sdwa v15, v2 dst_sel:DWORD dst_unused:UNUSED_PAD src0_sel:WORD_1
	v_cvt_f32_f16_e32 v16, v3
	v_cvt_f32_f16_sdwa v17, v3 dst_sel:DWORD dst_unused:UNUSED_PAD src0_sel:WORD_1
	v_cvt_f32_f16_e32 v19, v4
	v_cvt_f32_f16_sdwa v20, v4 dst_sel:DWORD dst_unused:UNUSED_PAD src0_sel:WORD_1
	v_cvt_f32_f16_e32 v21, v5
	v_cvt_f32_f16_sdwa v22, v5 dst_sel:DWORD dst_unused:UNUSED_PAD src0_sel:WORD_1
	v_max3_f32 v11, v13, 0, v15
	v_max3_f32 v11, v11, v16, v17
	v_max3_f32 v11, v11, v19, v20
	v_max3_f32 v11, v11, v21, v22
	s_nop 1
	v_mov_b32_dpp v18, v11 quad_perm:[1,0,3,2] row_mask:0xf bank_mask:0xf bound_ctrl:1
	v_max_f32_e32 v18, v18, v18
	v_max_f32_e32 v11, v11, v18
	s_nop 1
	v_mov_b32_dpp v18, v11 quad_perm:[2,3,0,1] row_mask:0xf bank_mask:0xf bound_ctrl:1
	v_max_f32_e32 v18, v18, v18
	v_max_f32_e32 v11, v11, v18
	s_nop 1
	v_mov_b32_dpp v18, v11 row_half_mirror row_mask:0xf bank_mask:0xf bound_ctrl:1
	v_max_f32_e32 v18, v18, v18
	v_max_f32_e32 v18, v11, v18
	v_mov_b32_e32 v11, 0x186a0
	v_cndmask_b32_e64 v12, v11, v12, s[0:1]
	v_mov_b32_dpp v23, v18 row_mirror row_mask:0xf bank_mask:0xf bound_ctrl:1
	v_cmp_gt_i32_e64 s[0:1], s4, v12
	s_and_saveexec_b64 s[2:3], s[0:1]
	s_cbranch_execz .LBB2_80
	v_max_f32_e32 v23, v23, v23
	v_max_f32_e32 v18, v18, v18
	v_max_f32_e32 v18, v18, v23
	v_rcp_f32_e32 v23, v18
	v_cmp_lt_f32_e64 s[0:1], 0, v18
	v_mul_f32_e32 v23, 0x437f0000, v23
	s_nop 0
	v_cndmask_b32_e64 v23, 0, v23, s[0:1]
	v_mul_f32_e32 v13, v23, v13
	v_mul_f32_e32 v19, v23, v19
	v_mul_f32_e32 v15, v23, v15
	v_rndne_f32_e32 v13, v13
	v_mul_f32_e32 v20, v23, v20
	v_rndne_f32_e32 v19, v19
	v_mul_f32_e32 v16, v23, v16
	v_rndne_f32_e32 v15, v15
	v_cvt_pk_u8_f32 v13, v13, 0, 0
	v_mul_f32_e32 v21, v23, v21
	v_rndne_f32_e32 v20, v20
	v_cvt_pk_u8_f32 v19, v19, 0, 0
	v_mul_f32_e32 v17, v23, v17
	v_rndne_f32_e32 v16, v16
	v_cvt_pk_u8_f32 v13, v15, 1, v13
	v_mul_f32_e32 v22, v23, v22
	v_rndne_f32_e32 v21, v21
	v_cvt_pk_u8_f32 v19, v20, 1, v19
	v_rndne_f32_e32 v17, v17
	v_cvt_pk_u8_f32 v13, v16, 2, v13
	v_rndne_f32_e32 v22, v22
	v_cvt_pk_u8_f32 v19, v21, 2, v19
	v_cvt_pk_u8_f32 v20, v17, 3, v13
	v_ashrrev_i32_e32 v13, 31, v12
	v_cvt_pk_u8_f32 v21, v22, 3, v19
	v_lshlrev_b64 v[22:23], 8, v[12:13]
	v_lshlrev_b64 v[16:17], 7, v[12:13]
	v_lshl_add_u64 v[22:23], v[8:9], 0, v[22:23]
	global_store_dwordx4 v[22:23], v[2:5], off
	s_nop 1
	v_lshl_add_u64 v[2:3], v[6:7], 0, v[16:17]
	global_store_dwordx2 v[2:3], v[20:21], off
	s_and_b64 exec, exec, vcc
	s_cbranch_execz .LBB2_80
	v_lshl_add_u64 v[2:3], v[12:13], 2, s[14:15]
	v_mul_f32_e32 v4, 0x40808081, v18
	global_store_dword v[2:3], v4, off
.LBB2_80:
	s_or_b64 exec, exec, s[2:3]
	v_add3_u32 v1, v14, v1, 48
	v_min_i32_e32 v2, 59, v1
	v_mad_u32_u24 v2, v2, s5, v10
	ds_read_b128 v[2:5], v2
	v_add_u32_e32 v20, s18, v1
	s_movk_i32 s0, 0xc0
	v_cmp_gt_u32_e64 s[0:1], s0, v0
	s_waitcnt lgkmcnt(0)
	v_cvt_f32_f16_e32 v1, v2
	v_cvt_f32_f16_sdwa v10, v2 dst_sel:DWORD dst_unused:UNUSED_PAD src0_sel:WORD_1
	v_cvt_f32_f16_e32 v12, v3
	v_cvt_f32_f16_sdwa v13, v3 dst_sel:DWORD dst_unused:UNUSED_PAD src0_sel:WORD_1
	v_cvt_f32_f16_e32 v14, v4
	v_cvt_f32_f16_sdwa v15, v4 dst_sel:DWORD dst_unused:UNUSED_PAD src0_sel:WORD_1
	v_cvt_f32_f16_e32 v16, v5
	v_cvt_f32_f16_sdwa v17, v5 dst_sel:DWORD dst_unused:UNUSED_PAD src0_sel:WORD_1
	v_max3_f32 v18, v1, 0, v10
	v_max3_f32 v18, v18, v12, v13
	v_max3_f32 v18, v18, v14, v15
	v_max3_f32 v18, v18, v16, v17
	v_cndmask_b32_e64 v0, v11, v20, s[0:1]
	v_cmp_gt_i32_e64 s[0:1], s4, v0
	v_mov_b32_dpp v19, v18 quad_perm:[1,0,3,2] row_mask:0xf bank_mask:0xf bound_ctrl:1
	v_max_f32_e32 v19, v19, v19
	v_max_f32_e32 v18, v18, v19
	s_nop 1
	v_mov_b32_dpp v19, v18 quad_perm:[2,3,0,1] row_mask:0xf bank_mask:0xf bound_ctrl:1
	v_max_f32_e32 v19, v19, v19
	v_max_f32_e32 v18, v18, v19
	s_nop 1
	v_mov_b32_dpp v19, v18 row_half_mirror row_mask:0xf bank_mask:0xf bound_ctrl:1
	v_max_f32_e32 v19, v19, v19
	v_max_f32_e32 v18, v18, v19
	s_nop 1
	v_mov_b32_dpp v19, v18 row_mirror row_mask:0xf bank_mask:0xf bound_ctrl:1
	s_and_saveexec_b64 s[2:3], s[0:1]
	s_cbranch_execz .LBB2_83
	v_max_f32_e32 v11, v19, v19
	v_max_f32_e32 v18, v18, v18
	v_max_f32_e32 v11, v18, v11
	v_rcp_f32_e32 v18, v11
	v_cmp_lt_f32_e64 s[0:1], 0, v11
	v_mul_f32_e32 v18, 0x437f0000, v18
	s_nop 0
	v_cndmask_b32_e64 v18, 0, v18, s[0:1]
	v_mul_f32_e32 v14, v18, v14
	v_mul_f32_e32 v1, v18, v1
	v_mul_f32_e32 v15, v18, v15
	v_rndne_f32_e32 v14, v14
	v_mul_f32_e32 v10, v18, v10
	v_rndne_f32_e32 v1, v1
	v_mul_f32_e32 v16, v18, v16
	v_rndne_f32_e32 v15, v15
	v_cvt_pk_u8_f32 v14, v14, 0, 0
	v_mul_f32_e32 v12, v18, v12
	v_rndne_f32_e32 v10, v10
	v_cvt_pk_u8_f32 v1, v1, 0, 0
	v_mul_f32_e32 v17, v18, v17
	v_rndne_f32_e32 v16, v16
	v_cvt_pk_u8_f32 v14, v15, 1, v14
	v_mul_f32_e32 v13, v18, v13
	v_rndne_f32_e32 v12, v12
	v_cvt_pk_u8_f32 v1, v10, 1, v1
	v_rndne_f32_e32 v17, v17
	v_cvt_pk_u8_f32 v14, v16, 2, v14
	v_rndne_f32_e32 v13, v13
	v_cvt_pk_u8_f32 v1, v12, 2, v1
	v_cvt_pk_u8_f32 v15, v17, 3, v14
	v_cvt_pk_u8_f32 v14, v13, 3, v1
	v_ashrrev_i32_e32 v1, 31, v0
	v_lshlrev_b64 v[16:17], 8, v[0:1]
	v_lshlrev_b64 v[12:13], 7, v[0:1]
	v_lshl_add_u64 v[8:9], v[8:9], 0, v[16:17]
	global_store_dwordx4 v[8:9], v[2:5], off
	s_nop 1
	v_lshl_add_u64 v[2:3], v[6:7], 0, v[12:13]
	global_store_dwordx2 v[2:3], v[14:15], off
	s_and_b64 exec, exec, vcc
	s_cbranch_execz .LBB2_83
	v_lshl_add_u64 v[0:1], v[0:1], 2, s[14:15]
	v_mul_f32_e32 v2, 0x40808081, v11
	global_store_dword v[0:1], v2, off

.LBB2_84:
	s_setprio 2
	v_add_u32_e32 v12, v78, v1
	v_add_u32_e32 v11, 4, v12
	v_add_u32_e32 v13, 8, v12
	v_add_u32_e32 v10, 12, v12
	v_min_i32_e32 v12, 0x1869f, v12
	v_min_i32_e32 v11, 0x1869f, v11
	v_min_i32_e32 v13, 0x1869f, v13
	v_min_i32_e32 v10, 0x1869f, v10
	v_lshl_or_b32 v46, v12, 9, v6
	v_lshl_or_b32 v47, v11, 9, v6
	v_lshl_or_b32 v48, v13, 9, v6
	v_lshl_or_b32 v49, v10, 9, v6
	global_load_dwordx4 v[2:5], v46, s[8:9]
	global_load_dwordx4 v[6:9], v46, s[8:9] offset:16
	global_load_dwordx4 v[14:17], v47, s[8:9]
	global_load_dwordx4 v[78:81], v47, s[8:9] offset:16
	global_load_dwordx4 v[82:85], v48, s[8:9]
	global_load_dwordx4 v[86:89], v48, s[8:9] offset:16
	global_load_dwordx4 v[90:93], v49, s[8:9]
	global_load_dwordx4 v[10:13], v49, s[8:9] offset:16
	s_cmp_gt_i32 s17, 3
	s_cbranch_scc1 .LBB2_105
	s_waitcnt vmcnt(18)
	s_mov_b32 s2, 0xc040c00
	v_cvt_pk_f16_f32 v46, v61, v62
	v_perm_b32 v47, v40, v38, s2
	s_mov_b32 s3, 0xc050c01
	v_dot2c_f32_f16_e32 v60, v47, v46
	v_perm_b32 v47, v40, v38, s3
	s_mov_b32 s8, 0xc060c02
	s_mov_b32 s9, 0xc070c03
	v_dot2c_f32_f16_e32 v42, v47, v46
	v_perm_b32 v47, v40, v38, s8
	v_perm_b32 v38, v40, v38, s9
	v_dot2c_f32_f16_e32 v36, v38, v46
	v_perm_b32 v38, v41, v39, s2
	v_dot2c_f32_f16_e32 v37, v38, v46
	v_perm_b32 v38, v41, v39, s3
	v_dot2c_f32_f16_e32 v30, v38, v46
	v_perm_b32 v38, v41, v39, s8
	v_dot2c_f32_f16_e32 v31, v38, v46
	v_perm_b32 v38, v41, v39, s9
	v_dot2c_f32_f16_e32 v53, v38, v46
	s_waitcnt vmcnt(16)
	v_cvt_pk_f16_f32 v38, v58, v59
	v_perm_b32 v39, v34, v32, s2
	v_dot2c_f32_f16_e32 v60, v39, v38
	v_perm_b32 v39, v34, v32, s3
	v_dot2c_f32_f16_e32 v42, v39, v38
	v_perm_b32 v39, v34, v32, s8
	v_perm_b32 v32, v34, v32, s9
	v_dot2c_f32_f16_e32 v36, v32, v38
	v_perm_b32 v32, v35, v33, s2
	v_dot2c_f32_f16_e32 v37, v32, v38
	v_perm_b32 v32, v35, v33, s3
	v_dot2c_f32_f16_e32 v30, v32, v38
	v_perm_b32 v32, v35, v33, s8
	v_dot2c_f32_f16_e32 v43, v47, v46
	v_dot2c_f32_f16_e32 v45, 0x3c003c00, v46
	v_dot2c_f32_f16_e32 v31, v32, v38
	v_perm_b32 v32, v35, v33, s9
	s_add_i32 s5, s5, 1
	v_dot2c_f32_f16_e32 v43, v39, v38
	v_dot2c_f32_f16_e32 v53, v32, v38
	v_dot2c_f32_f16_e32 v45, 0x3c003c00, v38
	s_cmp_lg_u32 s5, s4
	s_mov_b64 s[2:3], -1
	s_cbranch_scc1 .LBB2_102
	v_cmp_gt_i32_e32 vcc, 15, v18
	s_and_saveexec_b64 s[2:3], vcc
	s_cbranch_execz .LBB2_96
	v_max_i32_e32 v32, 1, v44
	v_cvt_f32_u32_e32 v32, v32
	s_mov_b32 s4, 0x3a800000
	s_mov_b32 s5, 0xc3000000
	v_add_u32_e32 v18, v18, v77
	v_rcp_iflag_f32_e32 v44, v32
	s_nop 0
	v_pk_mul_f32 v[32:33], v[44:45], s[4:5]
	s_nop 0
	v_mul_f32_e32 v38, 0x4b800000, v32
	v_pk_mul_f32 v[40:41], v[32:33], v[32:33] op_sel:[0,1] op_sel_hi:[1,0]
	s_nop 0
	v_fma_mixlo_f16 v39, v60, v38, v40
	v_pk_fma_f32 v[32:33], v[42:43], v[38:39], v[40:41] op_sel_hi:[1,0,0]
	v_pk_fma_f32 v[34:35], v[36:37], v[38:39], v[40:41] op_sel_hi:[1,0,0]
	v_pk_fma_f32 v[30:31], v[30:31], v[38:39], v[40:41] op_sel_hi:[1,0,0]
	v_cvt_pk_f16_f32 v33, v32, v33
	v_cvt_pk_f16_f32 v34, v34, v35
	v_cvt_pk_f16_f32 v30, v30, v31
	v_pack_b32_f16 v32, v39, v33
	v_alignbit_b32 v33, v34, v33, 16
	v_alignbit_b32 v34, v30, v34, 16
	v_lshrrev_b32_e32 v35, 16, v30
	v_xor_b32_e32 v30, v18, v0
	v_lshlrev_b32_e32 v30, 4, v30
	v_and_b32_e32 v30, 0xf0, v30
	v_fma_mixhi_f16 v35, v53, v38, v40
	v_lshl_or_b32 v18, v18, 8, v30
	ds_write_b128 v18, v[32:35]

.LBB2_102:
	s_add_i32 s5, s5, 1
	s_cmp_eq_u32 s5, s4
	s_cselect_b64 s[4:5], -1, 0
	s_and_b64 s[2:3], s[2:3], s[4:5]
	v_cmp_gt_i32_e32 vcc, 15, v18
	s_and_b64 s[4:5], s[2:3], vcc
	s_and_saveexec_b64 s[2:3], s[4:5]
	s_cbranch_execz .LBB2_104
	v_max_i32_e32 v33, 1, v44
	v_cvt_f32_u32_e32 v33, v33
	s_waitcnt vmcnt(8)
	v_cvt_pk_f16_f32 v39, v54, v55
	v_rcp_iflag_f32_e32 v44, v33
	v_cvt_pk_f16_f32 v40, v56, v57
	s_mov_b32 s6, 0xc040c00
	v_dot2c_f32_f16_e32 v45, 0x3c003c00, v40
	s_mov_b32 s4, 0x3a800000
	v_perm_b32 v20, v28, v26, s6
	v_dot2c_f32_f16_e32 v45, 0x3c003c00, v39
	s_mov_b32 s5, 0xc3000000
	v_dot2c_f32_f16_e32 v60, v20, v40
	v_perm_b32 v19, v24, v22, s6
	v_pk_mul_f32 v[20:21], v[44:45], s[4:5]
	s_mov_b32 s4, 0xc050c01
	v_perm_b32 v33, v28, v26, s4
	s_mov_b32 s5, 0xc060c02
	v_perm_b32 v32, v24, v22, s4
	v_dot2c_f32_f16_e32 v42, v33, v40
	v_perm_b32 v33, v28, v26, s5
	v_dot2c_f32_f16_e32 v42, v32, v39
	v_perm_b32 v32, v24, v22, s5
	v_dot2c_f32_f16_e32 v43, v33, v40
	v_mul_f32_e32 v38, 0x4b800000, v20
	v_pk_mul_f32 v[20:21], v[20:21], v[20:21] op_sel:[0,1] op_sel_hi:[1,0]
	v_dot2c_f32_f16_e32 v43, v32, v39
	v_dot2c_f32_f16_e32 v60, v19, v39
	s_mov_b32 s7, 0xc070c03
	v_add_u32_e32 v18, v18, v77
	v_pk_fma_f32 v[32:33], v[42:43], v[38:39], v[20:21] op_sel_hi:[1,0,0]
	v_fma_mixlo_f16 v19, v60, v38, v20
	v_cvt_pk_f16_f32 v33, v32, v33
	v_pack_b32_f16 v32, v19, v33
	v_perm_b32 v19, v24, v22, s7
	v_perm_b32 v22, v28, v26, s7
	v_dot2c_f32_f16_e32 v36, v22, v40
	v_perm_b32 v22, v29, v27, s6
	v_perm_b32 v24, v29, v27, s4
	v_dot2c_f32_f16_e32 v37, v22, v40
	v_perm_b32 v22, v25, v23, s4
	v_dot2c_f32_f16_e32 v30, v24, v40
	v_perm_b32 v24, v29, v27, s5
	v_dot2c_f32_f16_e32 v36, v19, v39
	v_perm_b32 v19, v25, v23, s6
	v_dot2c_f32_f16_e32 v30, v22, v39
	v_perm_b32 v22, v25, v23, s5
	v_dot2c_f32_f16_e32 v31, v24, v40
	v_dot2c_f32_f16_e32 v37, v19, v39
	v_dot2c_f32_f16_e32 v31, v22, v39
	s_nop 1
	v_pk_fma_f32 v[34:35], v[36:37], v[38:39], v[20:21] op_sel_hi:[1,0,0]
	v_pk_fma_f32 v[30:31], v[30:31], v[38:39], v[20:21] op_sel_hi:[1,0,0]
	v_cvt_pk_f16_f32 v19, v34, v35
	v_cvt_pk_f16_f32 v21, v30, v31
	v_alignbit_b32 v34, v21, v19, 16
	v_lshrrev_b32_e32 v35, 16, v21
	v_perm_b32 v21, v29, v27, s7
	v_alignbit_b32 v33, v19, v33, 16
	v_perm_b32 v19, v25, v23, s7
	v_dot2c_f32_f16_e32 v53, v21, v40
	v_dot2c_f32_f16_e32 v53, v19, v39
	v_xor_b32_e32 v19, v18, v0
	v_lshlrev_b32_e32 v19, 4, v19
	v_and_b32_e32 v19, 0xf0, v19
	v_fma_mixhi_f16 v35, v53, v38, v20
	v_lshl_or_b32 v18, v18, 8, v19
	ds_write_b128 v18, v[32:35]

.LBB2_105:
	v_add_co_u32_e32 v18, vcc, 0x1000, v70
	s_nop 1
	v_addc_co_u32_e32 v19, vcc, 0, v71, vcc
	global_load_dwordx4 v[46:49], v[70:71], off
	global_load_dwordx4 v[34:37], v[18:19], off
	v_add_co_u32_e32 v18, vcc, 0x2000, v70
	s_nop 1
	v_addc_co_u32_e32 v19, vcc, 0, v71, vcc
	v_add_co_u32_e32 v20, vcc, 0x3000, v70
	s_nop 1
	v_addc_co_u32_e32 v21, vcc, 0, v71, vcc
	global_load_dwordx4 v[54:57], v[18:19], off
	global_load_dwordx4 v[38:41], v[20:21], off
	v_add_co_u32_e32 v18, vcc, 0x4000, v70
	s_nop 1
	v_addc_co_u32_e32 v19, vcc, 0, v71, vcc
	v_add_co_u32_e32 v20, vcc, 0x5000, v70
	s_nop 1
	v_addc_co_u32_e32 v21, vcc, 0, v71, vcc
	global_load_dwordx4 v[62:65], v[18:19], off
	global_load_dwordx4 v[42:45], v[20:21], off
	v_add_co_u32_e32 v18, vcc, 0x6000, v70
	s_nop 1
	v_addc_co_u32_e32 v19, vcc, 0, v71, vcc
	v_add_co_u32_e32 v20, vcc, 0x7000, v70
	s_nop 1
	v_addc_co_u32_e32 v21, vcc, 0, v71, vcc
	global_load_dwordx4 v[58:61], v[18:19], off
	global_load_dwordx4 v[50:53], v[20:21], off
	s_waitcnt vmcnt(8)
	v_cvt_pk_f16_f32 v2, v2, v3
	v_cvt_pk_f16_f32 v3, v4, v5
	v_cvt_pk_f16_f32 v4, v6, v7
	v_cvt_pk_f16_f32 v5, v8, v9
	v_cvt_pk_f16_f32 v14, v14, v15
	v_cvt_pk_f16_f32 v15, v16, v17
	v_cvt_pk_f16_f32 v16, v78, v79
	v_cvt_pk_f16_f32 v17, v80, v81
	v_cvt_pk_f16_f32 v82, v82, v83
	v_cvt_pk_f16_f32 v83, v84, v85
	v_cvt_pk_f16_f32 v84, v86, v87
	v_cvt_pk_f16_f32 v85, v88, v89
	v_cvt_pk_f16_f32 v90, v90, v91
	v_cvt_pk_f16_f32 v91, v92, v93
	v_cvt_pk_f16_f32 v92, v10, v11
	v_cvt_pk_f16_f32 v93, v12, v13
	v_xor_b32_e32 v18, v76, v0
	v_lshlrev_b32_e32 v18, 4, v18
	v_and_b32_e32 v18, 0xf0, v18
	v_lshl_or_b32 v18, v76, 8, v18
	ds_write_b128 v18, v[2:5] offset:15360
	v_add_u32_e32 v6, 4, v76
	v_xor_b32_e32 v7, v6, v0
	v_lshlrev_b32_e32 v7, 4, v7
	v_and_b32_e32 v7, 0xf0, v7
	v_lshl_or_b32 v6, v6, 8, v7
	ds_write_b128 v6, v[14:17] offset:15360
	v_add_u32_e32 v8, 8, v76
	v_xor_b32_e32 v9, v8, v0
	v_lshlrev_b32_e32 v9, 4, v9
	v_and_b32_e32 v9, 0xf0, v9
	v_lshl_or_b32 v8, v8, 8, v9
	v_cmp_ne_u32_e32 vcc, 3, v1
	ds_write_b128 v8, v[82:85] offset:15360
	s_and_saveexec_b64 s[2:3], vcc
	s_cbranch_execz .LBB2_107
	v_add_u32_e32 v10, 12, v76
	v_xor_b32_e32 v11, v10, v0
	v_lshlrev_b32_e32 v11, 4, v11
	v_and_b32_e32 v11, 0xf0, v11
	v_lshl_or_b32 v10, v10, 8, v11
	ds_write_b128 v10, v[90:93] offset:15360
.LBB2_107:
	s_or_b64 exec, exec, s[2:3]
	s_load_dwordx4 s[4:7], s[0:1], 0x38
	s_cmpk_lt_i32 s19, 0x181
	s_cbranch_scc0 .LBB2_62
	s_branch .LBB2_63
	s_nop 0
	s_nop 0
	s_nop 0
	s_nop 0
	s_nop 0
	s_nop 0
	s_endpgm

	.amdhsa_kernel _Z7k_layerILb1EEvPKvPKhPKfPKiS7_PKDF16_S5_PvPhPf
		.amdhsa_group_segment_fixed_size 30720
		.amdhsa_private_segment_fixed_size 0
		.amdhsa_kernarg_size 80
		.amdhsa_user_sgpr_count 2
		.amdhsa_user_sgpr_dispatch_ptr 0
		.amdhsa_user_sgpr_queue_ptr 0
		.amdhsa_user_sgpr_kernarg_segment_ptr 1
		.amdhsa_user_sgpr_dispatch_id 0
		.amdhsa_user_sgpr_kernarg_preload_length 0
		.amdhsa_user_sgpr_kernarg_preload_offset 0
		.amdhsa_user_sgpr_private_segment_size 0
		.amdhsa_uses_dynamic_stack 0
		.amdhsa_enable_private_segment 0
		.amdhsa_system_sgpr_workgroup_id_x 1
		.amdhsa_system_sgpr_workgroup_id_y 0
		.amdhsa_system_sgpr_workgroup_id_z 0
		.amdhsa_system_sgpr_workgroup_info 0
		.amdhsa_system_vgpr_workitem_id 0
		.amdhsa_next_free_vgpr 94
		.amdhsa_next_free_sgpr 96
		.amdhsa_accum_offset 96
		.amdhsa_reserve_vcc 1
		.amdhsa_float_round_mode_32 0
		.amdhsa_float_round_mode_16_64 0
		.amdhsa_float_denorm_mode_32 3
		.amdhsa_float_denorm_mode_16_64 3
		.amdhsa_dx10_clamp 1
		.amdhsa_ieee_mode 1
		.amdhsa_fp16_overflow 0
		.amdhsa_tg_split 0
		.amdhsa_exception_fp_ieee_invalid_op 0
		.amdhsa_exception_fp_denorm_src 0
		.amdhsa_exception_fp_ieee_div_zero 0
		.amdhsa_exception_fp_ieee_overflow 0
		.amdhsa_exception_fp_ieee_underflow 0
		.amdhsa_exception_fp_ieee_inexact 0
		.amdhsa_exception_int_div_zero 0
	.end_amdhsa_kernel

.Lfunc_end2:
	.size	_Z7k_layerILb1EEvPKvPKhPKfPKiS7_PKDF16_S5_PvPhPf, .Lfunc_end2-_Z7k_layerILb1EEvPKvPKhPKfPKiS7_PKDF16_S5_PvPhPf
	.set _Z7k_layerILb1EEvPKvPKhPKfPKiS7_PKDF16_S5_PvPhPf.num_vgpr, 94
	.set _Z7k_layerILb1EEvPKvPKhPKfPKiS7_PKDF16_S5_PvPhPf.num_agpr, 0
	.set _Z7k_layerILb1EEvPKvPKhPKfPKiS7_PKDF16_S5_PvPhPf.numbered_sgpr, 30
	.set _Z7k_layerILb1EEvPKvPKhPKfPKiS7_PKDF16_S5_PvPhPf.num_named_barrier, 0
	.set _Z7k_layerILb1EEvPKvPKhPKfPKiS7_PKDF16_S5_PvPhPf.private_seg_size, 0
	.set _Z7k_layerILb1EEvPKvPKhPKfPKiS7_PKDF16_S5_PvPhPf.uses_vcc, 1
	.set _Z7k_layerILb1EEvPKvPKhPKfPKiS7_PKDF16_S5_PvPhPf.uses_flat_scratch, 0
	.set _Z7k_layerILb1EEvPKvPKhPKfPKiS7_PKDF16_S5_PvPhPf.has_dyn_sized_stack, 0
	.set _Z7k_layerILb1EEvPKvPKhPKfPKiS7_PKDF16_S5_PvPhPf.has_recursion, 0
	.set _Z7k_layerILb1EEvPKvPKhPKfPKiS7_PKDF16_S5_PvPhPf.has_indirect_call, 0

.LBB3_8:
	v_add_u32_e32 v15, s19, v74
	v_add_u32_e32 v16, s16, v15
	v_min_i32_e32 v16, 0x186a0, v16
	v_lshl_or_b32 v16, v16, 8, v77
	global_load_dwordx4 v[26:29], v16, s[8:9]
	v_max_i32_e32 v16, 1, v25
	v_cvt_f32_u32_e32 v16, v16
	v_pk_add_f32 v[6:7], v[6:7], v[14:15] op_sel_hi:[1,0] neg_lo:[0,1] neg_hi:[0,1]
	v_pk_add_f32 v[12:13], v[12:13], v[14:15] op_sel_hi:[1,0] neg_lo:[0,1] neg_hi:[0,1]
	v_pk_add_f32 v[10:11], v[10:11], v[14:15] op_sel_hi:[1,0] neg_lo:[0,1] neg_hi:[0,1]
	v_div_scale_f32 v17, s[14:15], v16, v16, 1.0
	v_rcp_f32_e32 v25, v17
	v_pk_add_f32 v[8:9], v[8:9], v[14:15] op_sel_hi:[1,0] neg_lo:[0,1] neg_hi:[0,1]
	v_fma_f32 v30, -v17, v25, 1.0
	v_fmac_f32_e32 v25, v30, v25
	v_div_scale_f32 v30, vcc, 1.0, v16, 1.0
	v_mul_f32_e32 v31, v30, v25
	v_fma_f32 v32, -v17, v31, v30
	v_fmac_f32_e32 v31, v32, v25
	v_fma_f32 v17, -v17, v31, v30
	v_div_fmas_f32 v17, v17, v25, v31
	v_div_fixup_f32 v16, v17, v16, 1.0
	v_mul_f32_e32 v16, 0x3a800000, v16
	v_pk_mul_f32 v[6:7], v[16:17], v[6:7] op_sel_hi:[0,1]
	v_cvt_pk_f16_f32 v33, v6, v7
	v_xor_b32_e32 v6, v15, v0
	v_lshlrev_b32_e32 v6, 4, v6
	v_pk_mul_f32 v[12:13], v[16:17], v[12:13] op_sel_hi:[0,1]
	v_pk_mul_f32 v[10:11], v[16:17], v[10:11] op_sel_hi:[0,1]
	v_pk_mul_f32 v[8:9], v[16:17], v[8:9] op_sel_hi:[0,1]
	v_and_b32_e32 v6, 0xf0, v6
	v_cvt_pk_f16_f32 v30, v12, v13
	v_cvt_pk_f16_f32 v31, v10, v11
	v_cvt_pk_f16_f32 v32, v8, v9
	v_lshl_or_b32 v6, v15, 8, v6
	ds_write_b128 v6, v[30:33]
	s_waitcnt vmcnt(0)
	ds_write_b128 v6, v[26:29] offset:15360
	s_branch .LBB3_2

.LBB3_33:
	s_waitcnt vmcnt(10)
	v_cvt_pk_f16_f32 v9, v57, v58
	v_perm_b32 v10, v40, v38, s21
	v_dot2c_f32_f16_e32 v56, v10, v9
	v_perm_b32 v10, v40, v38, s22
	v_dot2c_f32_f16_e32 v42, v10, v9
	v_perm_b32 v10, v40, v38, s23
	v_dot2c_f32_f16_e32 v43, v10, v9
	v_perm_b32 v10, v40, v38, s24
	v_dot2c_f32_f16_e32 v36, v10, v9
	v_perm_b32 v10, v41, v39, s21
	v_dot2c_f32_f16_e32 v37, v10, v9
	v_perm_b32 v10, v41, v39, s22
	v_dot2c_f32_f16_e32 v30, v10, v9
	v_perm_b32 v10, v41, v39, s23
	v_dot2c_f32_f16_e32 v31, v10, v9
	v_perm_b32 v10, v41, v39, s24
	v_dot2c_f32_f16_e32 v49, v10, v9
	s_waitcnt vmcnt(8)
	v_cvt_pk_f16_f32 v9, v54, v55
	v_perm_b32 v10, v34, v32, s21
	v_dot2c_f32_f16_e32 v56, v10, v9
	v_perm_b32 v10, v34, v32, s22
	v_dot2c_f32_f16_e32 v42, v10, v9
	v_perm_b32 v10, v34, v32, s23
	v_dot2c_f32_f16_e32 v43, v10, v9
	v_perm_b32 v10, v34, v32, s24
	v_dot2c_f32_f16_e32 v36, v10, v9
	v_perm_b32 v10, v35, v33, s21
	v_dot2c_f32_f16_e32 v37, v10, v9
	v_perm_b32 v10, v35, v33, s22
	v_dot2c_f32_f16_e32 v30, v10, v9
	v_perm_b32 v10, v35, v33, s23
	v_dot2c_f32_f16_e32 v31, v10, v9
	v_perm_b32 v10, v35, v33, s24
	s_add_i32 s5, s5, 1
	v_dot2c_f32_f16_e32 v49, v10, v9
	s_cmp_lg_u32 s5, s4
	s_cbranch_scc1 .LBB3_41
	v_cmp_gt_i32_e32 vcc, 15, v18
	s_and_saveexec_b64 s[4:5], vcc
	s_cbranch_execz .LBB3_36
	v_max_i32_e32 v9, 1, v44
	v_cvt_f32_u32_e32 v9, v9
	v_rcp_iflag_f32_e32 v44, v9
	s_nop 0
	v_pk_mul_f32 v[10:11], v[44:45], s[2:3]
	s_nop 0
	v_mul_f32_e32 v14, 0x4b800000, v10
	v_pk_mul_f32 v[16:17], v[10:11], v[10:11] op_sel:[0,1] op_sel_hi:[1,0]
	s_nop 0
	v_pk_fma_f32 v[10:11], v[42:43], v[14:15], v[16:17] op_sel_hi:[1,0,0]
	v_fma_mixlo_f16 v9, v56, v14, v16
	v_pk_fma_f32 v[12:13], v[36:37], v[14:15], v[16:17] op_sel_hi:[1,0,0]
	v_pk_fma_f32 v[30:31], v[30:31], v[14:15], v[16:17] op_sel_hi:[1,0,0]
	v_cvt_pk_f16_f32 v11, v10, v11
	v_cvt_pk_f16_f32 v12, v12, v13
	v_pack_b32_f16 v10, v9, v11
	v_cvt_pk_f16_f32 v9, v30, v31
	v_alignbit_b32 v11, v12, v11, 16
	v_alignbit_b32 v12, v9, v12, 16
	v_lshrrev_b32_e32 v13, 16, v9
	v_add_u32_e32 v9, v18, v75
	v_fma_mixhi_f16 v13, v49, v14, v16
	v_xor_b32_e32 v14, v9, v0
	v_lshlrev_b32_e32 v14, 4, v14
	v_and_b32_e32 v14, 0xf0, v14
	v_lshl_or_b32 v9, v9, 8, v14
	ds_write_b128 v9, v[10:13]

.LBB3_41:
	s_lshl_b32 s26, s25, 2
	v_add_u32_e32 v9, s26, v3
	v_lshl_add_u32 v9, v9, 2, v2
	ds_read_b32 v10, v9 offset:15360
	ds_read_b32 v11, v9 offset:15364
	ds_read_b32 v12, v9 offset:15368
	ds_read_b32 v9, v9 offset:15372
	v_cmp_lt_i32_e32 vcc, s26, v5
	s_or_b32 s27, s26, 1
	s_add_i32 s25, s25, 1
	s_waitcnt lgkmcnt(3)
	v_cndmask_b32_e32 v10, v8, v10, vcc
	v_cmp_lt_i32_e32 vcc, s27, v5
	s_or_b32 s27, s26, 2
	s_or_b32 s26, s26, 3
	s_waitcnt lgkmcnt(2)
	v_cndmask_b32_e32 v11, v8, v11, vcc
	v_cmp_lt_i32_e32 vcc, s27, v5
	v_lshl_or_b32 v13, v10, 7, v78
	v_lshlrev_b32_e32 v10, 2, v10
	s_waitcnt lgkmcnt(1)
	v_cndmask_b32_e32 v12, v8, v12, vcc
	v_cmp_lt_i32_e32 vcc, s26, v5
	v_lshl_or_b32 v14, v11, 7, v78
	v_lshl_or_b32 v15, v12, 7, v78
	s_waitcnt lgkmcnt(0)
	v_cndmask_b32_e32 v9, v8, v9, vcc
	v_lshl_or_b32 v16, v9, 7, v78
	global_load_dwordx2 v[38:39], v13, s[10:11]
	global_load_dwordx2 v[40:41], v14, s[10:11]
	global_load_dwordx2 v[32:33], v15, s[10:11]
	global_load_dwordx2 v[34:35], v16, s[10:11]
	v_lshlrev_b32_e32 v11, 2, v11
	v_lshlrev_b32_e32 v12, 2, v12
	v_lshlrev_b32_e32 v9, 2, v9
	global_load_dword v57, v10, s[12:13]
	global_load_dword v58, v11, s[12:13]
	global_load_dword v54, v12, s[12:13]
	global_load_dword v55, v9, s[12:13]
	s_cmp_lg_u32 s25, s19
	s_cbranch_scc1 .LBB3_47
	s_cmp_eq_u32 s7, 0
	s_cbranch_scc1 .LBB3_45
	s_add_i32 s25, s7, 1
	s_mov_b32 s7, 2
	s_cmp_eq_u32 s25, 2
	v_mov_b32_e32 v3, v6
	v_mov_b32_e32 v5, v47
	s_mov_b32 s19, s15
	s_cbranch_scc1 .LBB3_46
	s_cmp_eq_u32 s25, 3
	s_cselect_b64 vcc, -1, 0
	s_and_b64 s[26:27], vcc, exec
	v_cndmask_b32_e32 v5, 0, v48, vcc
	s_cselect_b32 s19, s6, 0x7fffffff
	s_mov_b32 s7, s25
	v_mov_b32_e32 v3, v7
	s_branch .LBB3_46

.LBB3_47:
	s_waitcnt vmcnt(10)
	v_cvt_pk_f16_f32 v9, v52, v53
	v_perm_b32 v10, v28, v26, s21
	v_dot2c_f32_f16_e32 v56, v10, v9
	v_perm_b32 v10, v28, v26, s22
	v_dot2c_f32_f16_e32 v42, v10, v9
	v_perm_b32 v10, v28, v26, s23
	v_dot2c_f32_f16_e32 v43, v10, v9
	v_perm_b32 v10, v28, v26, s24
	v_dot2c_f32_f16_e32 v36, v10, v9
	v_perm_b32 v10, v29, v27, s21
	v_dot2c_f32_f16_e32 v37, v10, v9
	v_perm_b32 v10, v29, v27, s22
	v_dot2c_f32_f16_e32 v30, v10, v9
	v_perm_b32 v10, v29, v27, s23
	v_dot2c_f32_f16_e32 v31, v10, v9
	v_perm_b32 v10, v29, v27, s24
	v_dot2c_f32_f16_e32 v49, v10, v9
	s_waitcnt vmcnt(8)
	v_cvt_pk_f16_f32 v9, v50, v51
	v_perm_b32 v10, v24, v22, s21
	v_dot2c_f32_f16_e32 v56, v10, v9
	v_perm_b32 v10, v24, v22, s22
	v_dot2c_f32_f16_e32 v42, v10, v9
	v_perm_b32 v10, v24, v22, s23
	v_dot2c_f32_f16_e32 v43, v10, v9
	v_perm_b32 v10, v24, v22, s24
	v_dot2c_f32_f16_e32 v36, v10, v9
	v_perm_b32 v10, v25, v23, s21
	v_dot2c_f32_f16_e32 v37, v10, v9
	v_perm_b32 v10, v25, v23, s22
	v_dot2c_f32_f16_e32 v30, v10, v9
	v_perm_b32 v10, v25, v23, s23
	v_dot2c_f32_f16_e32 v31, v10, v9
	v_perm_b32 v10, v25, v23, s24
	s_add_i32 s5, s5, 1
	v_dot2c_f32_f16_e32 v49, v10, v9
	s_cmp_lg_u32 s5, s4
	s_cbranch_scc1 .LBB3_55
	v_cmp_gt_i32_e32 vcc, 15, v18
	s_and_saveexec_b64 s[4:5], vcc
	s_cbranch_execz .LBB3_50
	v_max_i32_e32 v9, 1, v44
	v_cvt_f32_u32_e32 v9, v9
	v_rcp_iflag_f32_e32 v44, v9
	s_nop 0
	v_pk_mul_f32 v[10:11], v[44:45], s[2:3]
	s_nop 0
	v_mul_f32_e32 v14, 0x4b800000, v10
	v_pk_mul_f32 v[16:17], v[10:11], v[10:11] op_sel:[0,1] op_sel_hi:[1,0]
	s_nop 0
	v_pk_fma_f32 v[10:11], v[42:43], v[14:15], v[16:17] op_sel_hi:[1,0,0]
	v_fma_mixlo_f16 v9, v56, v14, v16
	v_pk_fma_f32 v[12:13], v[36:37], v[14:15], v[16:17] op_sel_hi:[1,0,0]
	v_pk_fma_f32 v[22:23], v[30:31], v[14:15], v[16:17] op_sel_hi:[1,0,0]
	v_cvt_pk_f16_f32 v11, v10, v11
	v_cvt_pk_f16_f32 v12, v12, v13
	v_pack_b32_f16 v10, v9, v11
	v_cvt_pk_f16_f32 v9, v22, v23
	v_alignbit_b32 v11, v12, v11, 16
	v_alignbit_b32 v12, v9, v12, 16
	v_lshrrev_b32_e32 v13, 16, v9
	v_add_u32_e32 v9, v18, v75
	v_fma_mixhi_f16 v13, v49, v14, v16
	v_xor_b32_e32 v14, v9, v0
	v_lshlrev_b32_e32 v14, 4, v14
	v_and_b32_e32 v14, 0xf0, v14
	v_lshl_or_b32 v9, v9, 8, v14
	ds_write_b128 v9, v[10:13]

.LBB3_55:
	s_lshl_b32 s26, s25, 2
	v_add_u32_e32 v9, s26, v3
	v_lshl_add_u32 v9, v9, 2, v2
	ds_read_b32 v10, v9 offset:15360
	ds_read_b32 v11, v9 offset:15364
	ds_read_b32 v12, v9 offset:15368
	ds_read_b32 v9, v9 offset:15372
	v_cmp_lt_i32_e32 vcc, s26, v5
	s_or_b32 s27, s26, 1
	s_add_i32 s25, s25, 1
	s_waitcnt lgkmcnt(3)
	v_cndmask_b32_e32 v10, v8, v10, vcc
	v_cmp_lt_i32_e32 vcc, s27, v5
	s_or_b32 s27, s26, 2
	s_or_b32 s26, s26, 3
	s_waitcnt lgkmcnt(2)
	v_cndmask_b32_e32 v11, v8, v11, vcc
	v_cmp_lt_i32_e32 vcc, s27, v5
	v_lshl_or_b32 v13, v10, 7, v78
	v_lshlrev_b32_e32 v10, 2, v10
	s_waitcnt lgkmcnt(1)
	v_cndmask_b32_e32 v12, v8, v12, vcc
	v_cmp_lt_i32_e32 vcc, s26, v5
	v_lshl_or_b32 v14, v11, 7, v78
	v_lshl_or_b32 v15, v12, 7, v78
	s_waitcnt lgkmcnt(0)
	v_cndmask_b32_e32 v9, v8, v9, vcc
	v_lshl_or_b32 v16, v9, 7, v78
	global_load_dwordx2 v[26:27], v13, s[10:11]
	global_load_dwordx2 v[28:29], v14, s[10:11]
	global_load_dwordx2 v[22:23], v15, s[10:11]
	global_load_dwordx2 v[24:25], v16, s[10:11]
	v_lshlrev_b32_e32 v11, 2, v11
	v_lshlrev_b32_e32 v12, 2, v12
	v_lshlrev_b32_e32 v9, 2, v9
	global_load_dword v52, v10, s[12:13]
	global_load_dword v53, v11, s[12:13]
	global_load_dword v50, v12, s[12:13]
	global_load_dword v51, v9, s[12:13]
	s_cmp_lg_u32 s25, s19
	s_cbranch_scc1 .LBB3_32
	s_cmp_eq_u32 s7, 0
	s_cbranch_scc1 .LBB3_30
	s_add_i32 s25, s7, 1
	s_mov_b32 s7, 2
	s_cmp_eq_u32 s25, 2
	v_mov_b32_e32 v3, v6
	v_mov_b32_e32 v5, v47
	s_mov_b32 s19, s15
	s_cbranch_scc1 .LBB3_31
	s_cmp_eq_u32 s25, 3
	s_cselect_b64 vcc, -1, 0
	s_and_b64 s[26:27], vcc, exec
	v_cndmask_b32_e32 v5, 0, v48, vcc
	s_cselect_b32 s19, s6, 0x7fffffff
	s_mov_b32 s7, s25
	v_mov_b32_e32 v3, v7
	s_branch .LBB3_31

.LBB3_86:
	s_setprio 2
	v_add_u32_e32 v2, v76, v73
	v_min_i32_e32 v3, 0x186a0, v2
	v_add_u32_e32 v4, 4, v2
	v_lshl_or_b32 v3, v3, 8, v77
	v_min_i32_e32 v4, 0x186a0, v4
	v_lshl_or_b32 v4, v4, 8, v77
	global_load_dwordx4 v[14:17], v3, s[8:9]
	global_load_dwordx4 v[6:9], v4, s[8:9]
	v_add_u32_e32 v3, 8, v2
	v_add_u32_e32 v2, 12, v2
	v_min_i32_e32 v3, 0x186a0, v3
	v_min_i32_e32 v2, 0x186a0, v2
	v_lshl_or_b32 v3, v3, 8, v77
	v_lshl_or_b32 v2, v2, 8, v77
	global_load_dwordx4 v[10:13], v3, s[8:9]
	s_nop 0
	global_load_dwordx4 v[2:5], v2, s[8:9]
	s_cmp_lt_i32 s18, 4
	s_cbranch_scc0 .LBB3_99
	s_waitcnt vmcnt(14)
	s_mov_b32 s2, 0xc040c00
	v_cvt_pk_f16_f32 v57, v57, v58
	v_perm_b32 v58, v40, v38, s2
	s_mov_b32 s3, 0xc050c01
	v_dot2c_f32_f16_e32 v56, v58, v57
	v_perm_b32 v58, v40, v38, s3
	s_mov_b32 s7, 0xc060c02
	s_mov_b32 s8, 0xc070c03
	v_dot2c_f32_f16_e32 v42, v58, v57
	v_perm_b32 v58, v40, v38, s7
	v_perm_b32 v38, v40, v38, s8
	v_dot2c_f32_f16_e32 v36, v38, v57
	v_perm_b32 v38, v41, v39, s2
	v_dot2c_f32_f16_e32 v37, v38, v57
	v_perm_b32 v38, v41, v39, s3
	v_dot2c_f32_f16_e32 v30, v38, v57
	v_perm_b32 v38, v41, v39, s7
	v_dot2c_f32_f16_e32 v31, v38, v57
	v_perm_b32 v38, v41, v39, s8
	v_dot2c_f32_f16_e32 v49, v38, v57
	s_waitcnt vmcnt(12)
	v_cvt_pk_f16_f32 v38, v54, v55
	v_perm_b32 v39, v34, v32, s2
	v_dot2c_f32_f16_e32 v56, v39, v38
	v_perm_b32 v39, v34, v32, s3
	v_dot2c_f32_f16_e32 v42, v39, v38
	v_perm_b32 v39, v34, v32, s7
	v_perm_b32 v32, v34, v32, s8
	v_dot2c_f32_f16_e32 v36, v32, v38
	v_perm_b32 v32, v35, v33, s2
	v_dot2c_f32_f16_e32 v37, v32, v38
	v_perm_b32 v32, v35, v33, s3
	v_dot2c_f32_f16_e32 v30, v32, v38
	v_perm_b32 v32, v35, v33, s7
	v_dot2c_f32_f16_e32 v43, v58, v57
	v_dot2c_f32_f16_e32 v31, v32, v38
	v_perm_b32 v32, v35, v33, s8
	s_add_i32 s5, s5, 1
	v_dot2c_f32_f16_e32 v43, v39, v38
	v_dot2c_f32_f16_e32 v49, v32, v38
	s_cmp_lg_u32 s5, s4
	s_mov_b64 s[2:3], -1
	s_cbranch_scc1 .LBB3_96
	v_cmp_gt_i32_e32 vcc, 15, v18
	s_and_saveexec_b64 s[2:3], vcc
	s_cbranch_execz .LBB3_90
	v_max_i32_e32 v32, 1, v44
	v_cvt_f32_u32_e32 v32, v32
	s_mov_b32 s4, 0x3a800000
	s_brev_b32 s5, 1
	v_add_u32_e32 v18, v18, v75
	v_rcp_iflag_f32_e32 v44, v32
	s_nop 0
	v_pk_mul_f32 v[32:33], v[44:45], s[4:5]
	s_nop 0
	v_mul_f32_e32 v38, 0x4b800000, v32
	v_pk_mul_f32 v[40:41], v[32:33], v[32:33] op_sel:[0,1] op_sel_hi:[1,0]
	s_nop 0
	v_fma_mixlo_f16 v39, v56, v38, v40
	v_pk_fma_f32 v[32:33], v[42:43], v[38:39], v[40:41] op_sel_hi:[1,0,0]
	v_pk_fma_f32 v[34:35], v[36:37], v[38:39], v[40:41] op_sel_hi:[1,0,0]
	v_pk_fma_f32 v[30:31], v[30:31], v[38:39], v[40:41] op_sel_hi:[1,0,0]
	v_cvt_pk_f16_f32 v33, v32, v33
	v_cvt_pk_f16_f32 v34, v34, v35
	v_cvt_pk_f16_f32 v30, v30, v31
	v_pack_b32_f16 v32, v39, v33
	v_alignbit_b32 v33, v34, v33, 16
	v_alignbit_b32 v34, v30, v34, 16
	v_lshrrev_b32_e32 v35, 16, v30
	v_xor_b32_e32 v30, v18, v0
	v_lshlrev_b32_e32 v30, 4, v30
	v_and_b32_e32 v30, 0xf0, v30
	v_fma_mixhi_f16 v35, v49, v38, v40
	v_lshl_or_b32 v18, v18, 8, v30
	ds_write_b128 v18, v[32:35]

.LBB3_96:
	s_add_i32 s5, s5, 1
	s_cmp_eq_u32 s5, s4
	s_cselect_b64 s[4:5], -1, 0
	s_and_b64 s[2:3], s[2:3], s[4:5]
	v_cmp_gt_i32_e32 vcc, 15, v18
	s_and_b64 s[4:5], s[2:3], vcc
	s_and_saveexec_b64 s[2:3], s[4:5]
	s_cbranch_execz .LBB3_98
	v_max_i32_e32 v33, 1, v44
	v_cvt_f32_u32_e32 v33, v33
	s_waitcnt vmcnt(4)
	v_cvt_pk_f16_f32 v39, v50, v51
	v_rcp_iflag_f32_e32 v44, v33
	v_cvt_pk_f16_f32 v40, v52, v53
	s_mov_b32 s6, 0xc040c00
	s_mov_b32 s4, 0x3a800000
	v_perm_b32 v20, v28, v26, s6
	s_brev_b32 s5, 1
	v_dot2c_f32_f16_e32 v56, v20, v40
	v_perm_b32 v19, v24, v22, s6
	v_pk_mul_f32 v[20:21], v[44:45], s[4:5]
	s_mov_b32 s4, 0xc050c01
	v_perm_b32 v33, v28, v26, s4
	s_mov_b32 s5, 0xc060c02
	v_perm_b32 v32, v24, v22, s4
	v_dot2c_f32_f16_e32 v42, v33, v40
	v_perm_b32 v33, v28, v26, s5
	v_dot2c_f32_f16_e32 v42, v32, v39
	v_perm_b32 v32, v24, v22, s5
	v_dot2c_f32_f16_e32 v43, v33, v40
	v_mul_f32_e32 v38, 0x4b800000, v20
	v_pk_mul_f32 v[20:21], v[20:21], v[20:21] op_sel:[0,1] op_sel_hi:[1,0]
	v_dot2c_f32_f16_e32 v43, v32, v39
	v_dot2c_f32_f16_e32 v56, v19, v39
	s_mov_b32 s7, 0xc070c03
	v_add_u32_e32 v18, v18, v75
	v_pk_fma_f32 v[32:33], v[42:43], v[38:39], v[20:21] op_sel_hi:[1,0,0]
	v_fma_mixlo_f16 v19, v56, v38, v20
	v_cvt_pk_f16_f32 v33, v32, v33
	v_pack_b32_f16 v32, v19, v33
	v_perm_b32 v19, v24, v22, s7
	v_perm_b32 v22, v28, v26, s7
	v_dot2c_f32_f16_e32 v36, v22, v40
	v_perm_b32 v22, v29, v27, s6
	v_perm_b32 v24, v29, v27, s4
	v_dot2c_f32_f16_e32 v37, v22, v40
	v_perm_b32 v22, v25, v23, s4
	v_dot2c_f32_f16_e32 v30, v24, v40
	v_perm_b32 v24, v29, v27, s5
	v_dot2c_f32_f16_e32 v36, v19, v39
	v_perm_b32 v19, v25, v23, s6
	v_dot2c_f32_f16_e32 v30, v22, v39
	v_perm_b32 v22, v25, v23, s5
	v_dot2c_f32_f16_e32 v31, v24, v40
	v_dot2c_f32_f16_e32 v37, v19, v39
	v_dot2c_f32_f16_e32 v31, v22, v39
	s_nop 1
	v_pk_fma_f32 v[34:35], v[36:37], v[38:39], v[20:21] op_sel_hi:[1,0,0]
	v_pk_fma_f32 v[30:31], v[30:31], v[38:39], v[20:21] op_sel_hi:[1,0,0]
	v_cvt_pk_f16_f32 v19, v34, v35
	v_cvt_pk_f16_f32 v21, v30, v31
	v_alignbit_b32 v34, v21, v19, 16
	v_lshrrev_b32_e32 v35, 16, v21
	v_perm_b32 v21, v29, v27, s7
	v_alignbit_b32 v33, v19, v33, 16
	v_perm_b32 v19, v25, v23, s7
	v_dot2c_f32_f16_e32 v49, v21, v40
	v_dot2c_f32_f16_e32 v49, v19, v39
	v_xor_b32_e32 v19, v18, v0
	v_lshlrev_b32_e32 v19, 4, v19
	v_and_b32_e32 v19, 0xf0, v19
	v_fma_mixhi_f16 v35, v49, v38, v20
	v_lshl_or_b32 v18, v18, 8, v19
	ds_write_b128 v18, v[32:35]

amdhsa.kernels:
  - .agpr_count:     0
    .args:
      - .actual_access:  read_only
        .address_space:  global
        .offset:         0
        .size:           8
        .value_kind:     global_buffer
      - .actual_access:  read_only
        .address_space:  global
        .offset:         8
        .size:           8
        .value_kind:     global_buffer
      - .actual_access:  read_only
        .address_space:  global
        .offset:         16
        .size:           8
        .value_kind:     global_buffer
      - .actual_access:  read_only
        .address_space:  global
        .offset:         24
        .size:           8
        .value_kind:     global_buffer
      - .actual_access:  read_only
        .address_space:  global
        .offset:         32
        .size:           8
        .value_kind:     global_buffer
      - .actual_access:  read_only
        .address_space:  global
        .offset:         40
        .size:           8
        .value_kind:     global_buffer
      - .actual_access:  read_only
        .address_space:  global
        .offset:         48
        .size:           8
        .value_kind:     global_buffer
      - .actual_access:  write_only
        .address_space:  global
        .offset:         56
        .size:           8
        .value_kind:     global_buffer
      - .actual_access:  write_only
        .address_space:  global
        .offset:         64
        .size:           8
        .value_kind:     global_buffer
      - .actual_access:  write_only
        .address_space:  global
        .offset:         72
        .size:           8
        .value_kind:     global_buffer
      - .actual_access:  write_only
        .address_space:  global
        .offset:         80
        .size:           8
        .value_kind:     global_buffer
      - .actual_access:  write_only
        .address_space:  global
        .offset:         88
        .size:           8
        .value_kind:     global_buffer
      - .actual_access:  write_only
        .address_space:  global
        .offset:         96
        .size:           8
        .value_kind:     global_buffer
      - .actual_access:  write_only
        .address_space:  global
        .offset:         104
        .size:           8
        .value_kind:     global_buffer
      - .actual_access:  write_only
        .address_space:  global
        .offset:         112
        .size:           8
        .value_kind:     global_buffer
      - .actual_access:  write_only
        .address_space:  global
        .offset:         120
        .size:           8
        .value_kind:     global_buffer
      - .actual_access:  write_only
        .address_space:  global
        .offset:         128
        .size:           8
        .value_kind:     global_buffer
      - .offset:         136
        .size:           4
        .value_kind:     hidden_block_count_x
      - .offset:         140
        .size:           4
        .value_kind:     hidden_block_count_y
      - .offset:         144
        .size:           4
        .value_kind:     hidden_block_count_z
      - .offset:         148
        .size:           2
        .value_kind:     hidden_group_size_x
      - .offset:         150
        .size:           2
        .value_kind:     hidden_group_size_y
      - .offset:         152
        .size:           2
        .value_kind:     hidden_group_size_z
      - .offset:         154
        .size:           2
        .value_kind:     hidden_remainder_x
      - .offset:         156
        .size:           2
        .value_kind:     hidden_remainder_y
      - .offset:         158
        .size:           2
        .value_kind:     hidden_remainder_z
      - .offset:         176
        .size:           8
        .value_kind:     hidden_global_offset_x
      - .offset:         184
        .size:           8
        .value_kind:     hidden_global_offset_y
      - .offset:         192
        .size:           8
        .value_kind:     hidden_global_offset_z
      - .offset:         200
        .size:           2
        .value_kind:     hidden_grid_dims
    .group_segment_fixed_size: 27136
    .kernarg_segment_align: 8
    .kernarg_segment_size: 392
    .language:       OpenCL C
    .language_version:
      - 2
      - 0
    .max_flat_workgroup_size: 1024
    .name:           _Z3k_APKfPKiS2_S0_S0_S0_S0_PDF16_S3_S3_S3_PiS4_PhS5_PfS6_
    .private_segment_fixed_size: 0
    .sgpr_count:     40
    .sgpr_spill_count: 0
    .symbol:         _Z3k_APKfPKiS2_S0_S0_S0_S0_PDF16_S3_S3_S3_PiS4_PhS5_PfS6_.kd
    .uniform_work_group_size: 1
    .uses_dynamic_stack: false
    .vgpr_count:     48
    .vgpr_spill_count: 0
    .wavefront_size: 64
  - .agpr_count:     0
    .args:
      - .actual_access:  read_only
        .address_space:  global
        .offset:         0
        .size:           8
        .value_kind:     global_buffer
      - .actual_access:  read_only
        .address_space:  global
        .offset:         8
        .size:           8
        .value_kind:     global_buffer
      - .actual_access:  write_only
        .address_space:  global
        .offset:         16
        .size:           8
        .value_kind:     global_buffer
      - .actual_access:  write_only
        .address_space:  global
        .offset:         24
        .size:           8
        .value_kind:     global_buffer
      - .actual_access:  read_only
        .address_space:  global
        .offset:         32
        .size:           8
        .value_kind:     global_buffer
      - .actual_access:  read_only
        .address_space:  global
        .offset:         40
        .size:           8
        .value_kind:     global_buffer
    .group_segment_fixed_size: 27720
    .kernarg_segment_align: 8
    .kernarg_segment_size: 48
    .language:       OpenCL C
    .language_version:
      - 2
      - 0
    .max_flat_workgroup_size: 1024
    .name:           _Z3k_BPKiS0_PiS1_PKfPDF16_
    .private_segment_fixed_size: 0
    .sgpr_count:     40
    .sgpr_spill_count: 0
    .symbol:         _Z3k_BPKiS0_PiS1_PKfPDF16_.kd
    .uniform_work_group_size: 1
    .uses_dynamic_stack: false
    .vgpr_count:     60
    .vgpr_spill_count: 0
    .wavefront_size: 64
  - .agpr_count:     0
    .args:
      - .actual_access:  read_only
        .address_space:  global
        .offset:         0
        .size:           8
        .value_kind:     global_buffer
      - .actual_access:  read_only
        .address_space:  global
        .offset:         8
        .size:           8
        .value_kind:     global_buffer
      - .actual_access:  read_only
        .address_space:  global
        .offset:         16
        .size:           8
        .value_kind:     global_buffer
      - .actual_access:  read_only
        .address_space:  global
        .offset:         24
        .size:           8
        .value_kind:     global_buffer
      - .actual_access:  read_only
        .address_space:  global
        .offset:         32
        .size:           8
        .value_kind:     global_buffer
      - .actual_access:  read_only
        .address_space:  global
        .offset:         40
        .size:           8
        .value_kind:     global_buffer
      - .actual_access:  read_only
        .address_space:  global
        .offset:         48
        .size:           8
        .value_kind:     global_buffer
      - .actual_access:  write_only
        .address_space:  global
        .offset:         56
        .size:           8
        .value_kind:     global_buffer
      - .actual_access:  write_only
        .address_space:  global
        .offset:         64
        .size:           8
        .value_kind:     global_buffer
      - .actual_access:  write_only
        .address_space:  global
        .offset:         72
        .size:           8
        .value_kind:     global_buffer
    .group_segment_fixed_size: 30720
    .kernarg_segment_align: 8
    .kernarg_segment_size: 80
    .language:       OpenCL C
    .language_version:
      - 2
      - 0
    .max_flat_workgroup_size: 256
    .name:           _Z7k_layerILb1EEvPKvPKhPKfPKiS7_PKDF16_S5_PvPhPf
    .private_segment_fixed_size: 0
    .sgpr_count:     36
    .sgpr_spill_count: 0
    .symbol:         _Z7k_layerILb1EEvPKvPKhPKfPKiS7_PKDF16_S5_PvPhPf.kd
    .uniform_work_group_size: 1
    .uses_dynamic_stack: false
    .vgpr_count:     94
    .vgpr_spill_count: 0
    .wavefront_size: 64
  - .agpr_count:     0
    .args:
      - .actual_access:  read_only
        .address_space:  global
        .offset:         0
        .size:           8
        .value_kind:     global_buffer
      - .actual_access:  read_only
        .address_space:  global
        .offset:         8
        .size:           8
        .value_kind:     global_buffer
      - .actual_access:  read_only
        .address_space:  global
        .offset:         16
        .size:           8
        .value_kind:     global_buffer
      - .actual_access:  read_only
        .address_space:  global
        .offset:         24
        .size:           8
        .value_kind:     global_buffer
      - .actual_access:  read_only
        .address_space:  global
        .offset:         32
        .size:           8
        .value_kind:     global_buffer
      - .actual_access:  read_only
        .address_space:  global
        .offset:         40
        .size:           8
        .value_kind:     global_buffer
      - .actual_access:  read_only
        .address_space:  global
        .offset:         48
        .size:           8
        .value_kind:     global_buffer
      - .actual_access:  write_only
        .address_space:  global
        .offset:         56
        .size:           8
        .value_kind:     global_buffer
      - .actual_access:  read_only
        .address_space:  global
        .offset:         64
        .size:           8
        .value_kind:     global_buffer
      - .actual_access:  read_only
        .address_space:  global
        .offset:         72
        .size:           8
        .value_kind:     global_buffer
    .group_segment_fixed_size: 30720
    .kernarg_segment_align: 8
    .kernarg_segment_size: 80
    .language:       OpenCL C
    .language_version:
      - 2
      - 0
    .max_flat_workgroup_size: 256
    .name:           _Z7k_layerILb0EEvPKvPKhPKfPKiS7_PKDF16_S5_PvPhPf
    .private_segment_fixed_size: 0
    .sgpr_count:     34
    .sgpr_spill_count: 0
    .symbol:         _Z7k_layerILb0EEvPKvPKhPKfPKiS7_PKDF16_S5_PvPhPf.kd
    .uniform_work_group_size: 1
    .uses_dynamic_stack: false
    .vgpr_count:     91
    .vgpr_spill_count: 0
    .wavefront_size: 64
